# gathers: priority drop moved from before the weight broadcast to after the first expert's FMAs
# speedup vs baseline: 1.0036x; 1.0027x over previous
.LBB0_763:
	s_cmpk_ge_i32 s58, 0x70
	s_cselect_b64 s[12:13], -1, 0
	ds_bpermute_b32 v84, v93, v92
	s_and_b64 vcc, s[12:13], s[48:49]
	v_cndmask_b32_e32 v104, v0, v94, vcc
	v_ashrrev_i32_e32 v105, 31, v104
	s_add_i32 s12, s58, 16
	s_and_b32 s12, s12, 0x70
	v_lshlrev_b64 v[104:105], 9, v[104:105]
	v_lshl_add_u64 v[104:105], s[94:95], 0, v[104:105]
	s_lshl_b32 s36, s12, 2
	s_waitcnt lgkmcnt(0)
	s_waitcnt vmcnt(32)
	v_mov_b32_e32 v92, v122
	v_ashrrev_i32_e32 v85, 31, v84
	v_lshl_add_u64 v[104:105], v[104:105], 0, s[36:37]
	v_lshl_add_u64 v[84:85], v[84:85], 3, s[8:9]
	v_lshl_add_u64 v[104:105], v[104:105], 0, v[144:145]
	global_load_dwordx2 v[84:85], v[84:85], off
	s_nop 0
	global_load_dword v86, v[72:73], off
	global_load_dword v122, v[104:105], off
	s_waitcnt vmcnt(19)
	v_dot8_i32_i4 v87, v8, v1, 0
	v_dot8_i32_i4 v104, v8, v88, 0
	v_dot8_i32_i4 v87, v9, v89, v87
	v_dot8_i32_i4 v104, v9, v90, v104
	s_waitcnt vmcnt(19)
	v_dot8_i32_i4 v9, v10, v88, 0
	v_dot8_i32_i4 v9, v11, v90, v9
	v_lshl_add_u32 v87, v87, 4, v104
	v_dot8_i32_i4 v8, v10, v1, 0
	v_dot8_i32_i4 v8, v11, v89, v8
	s_add_i32 s58, s58, 16
	v_lshl_add_u64 v[72:73], v[72:73], 0, 64
	s_nop 0
	v_lshl_add_u32 v104, v8, 4, v9
	v_dot8_i32_i4 v8, v12, v1, 0
	v_dot8_i32_i4 v9, v12, v88, 0
	v_dot8_i32_i4 v8, v13, v89, v8
	v_dot8_i32_i4 v9, v13, v90, v9
	v_readlane_b32 s12, v92, 0
	v_readlane_b32 s28, v92, 8
	v_readlane_b32 s30, v92, 9
	v_lshl_add_u32 v105, v8, 4, v9
	v_dot8_i32_i4 v8, v14, v1, 0
	v_dot8_i32_i4 v9, v14, v88, 0
	v_dot8_i32_i4 v8, v15, v89, v8
	v_dot8_i32_i4 v9, v15, v90, v9
	s_ashr_i32 s13, s12, 31
	v_readlane_b32 s14, v92, 1
	s_ashr_i32 s29, s28, 31
	v_lshl_add_u32 v106, v8, 4, v9
	v_dot8_i32_i4 v8, v16, v1, 0
	v_dot8_i32_i4 v9, v16, v88, 0
	v_dot8_i32_i4 v8, v17, v89, v8
	v_dot8_i32_i4 v9, v17, v90, v9
	s_ashr_i32 s31, s30, 31
	v_readlane_b32 s34, v92, 10
	s_lshl_b64 s[12:13], s[12:13], 9
	v_lshl_add_u32 v107, v8, 4, v9
	v_dot8_i32_i4 v8, v18, v1, 0
	v_dot8_i32_i4 v9, v18, v88, 0
	v_dot8_i32_i4 v8, v19, v89, v8
	v_dot8_i32_i4 v9, v19, v90, v9
	s_ashr_i32 s15, s14, 31
	v_readlane_b32 s16, v92, 2
	s_lshl_b64 s[28:29], s[28:29], 9
	v_lshl_add_u32 v108, v8, 4, v9
	v_dot8_i32_i4 v8, v20, v1, 0
	v_dot8_i32_i4 v9, v20, v88, 0
	v_dot8_i32_i4 v8, v21, v89, v8
	v_dot8_i32_i4 v9, v21, v90, v9
	s_lshl_b64 s[30:31], s[30:31], 9
	s_ashr_i32 s35, s34, 31
	v_readlane_b32 s38, v92, 11
	v_lshl_add_u32 v109, v8, 4, v9
	v_dot8_i32_i4 v8, v22, v1, 0
	v_dot8_i32_i4 v9, v22, v88, 0
	v_dot8_i32_i4 v8, v23, v89, v8
	v_dot8_i32_i4 v9, v23, v90, v9
	s_lshl_b64 s[14:15], s[14:15], 9
	s_ashr_i32 s17, s16, 31
	v_readlane_b32 s18, v92, 3
	v_lshl_add_u32 v110, v8, 4, v9
	v_dot8_i32_i4 v8, v24, v1, 0
	v_dot8_i32_i4 v9, v24, v88, 0
	v_dot8_i32_i4 v8, v25, v89, v8
	v_dot8_i32_i4 v9, v25, v90, v9
	s_lshl_b64 s[34:35], s[34:35], 9
	s_ashr_i32 s39, s38, 31
	s_nop 0
	v_lshl_add_u32 v111, v8, 4, v9
	v_dot8_i32_i4 v8, v38, v1, 0
	v_dot8_i32_i4 v9, v38, v88, 0
	v_dot8_i32_i4 v8, v39, v89, v8
	v_dot8_i32_i4 v9, v39, v90, v9
	s_setprio 2
	v_permlane32_swap_b32 v87, v111
	s_nop 1
	v_lshl_add_u32 v112, v8, 4, v9
	v_dot8_i32_i4 v8, v50, v1, 0
	v_dot8_i32_i4 v9, v50, v88, 0
	v_dot8_i32_i4 v8, v51, v89, v8
	v_dot8_i32_i4 v9, v51, v90, v9
	s_waitcnt lgkmcnt(0)
	v_add_u32_e32 v87, v87, v111
	v_permlane32_swap_b32 v104, v112
	v_lshl_add_u32 v113, v8, 4, v9
	v_dot8_i32_i4 v8, v48, v1, 0
	v_dot8_i32_i4 v9, v48, v88, 0
	v_dot8_i32_i4 v8, v49, v89, v8
	v_dot8_i32_i4 v9, v49, v90, v9
	s_waitcnt lgkmcnt(0)
	v_add_u32_e32 v104, v104, v112
	v_permlane32_swap_b32 v105, v113
	v_lshl_add_u32 v114, v8, 4, v9
	v_dot8_i32_i4 v8, v46, v1, 0
	v_dot8_i32_i4 v9, v46, v88, 0
	v_dot8_i32_i4 v8, v47, v89, v8
	v_dot8_i32_i4 v9, v47, v90, v9
	s_waitcnt lgkmcnt(0)
	v_add_u32_e32 v105, v105, v113
	v_permlane32_swap_b32 v106, v114
	v_lshl_add_u32 v115, v8, 4, v9
	v_dot8_i32_i4 v8, v44, v1, 0
	v_dot8_i32_i4 v9, v44, v88, 0
	v_dot8_i32_i4 v8, v45, v89, v8
	v_dot8_i32_i4 v9, v45, v90, v9
	s_waitcnt lgkmcnt(0)
	v_add_u32_e32 v106, v106, v114
	v_permlane32_swap_b32 v107, v115
	v_lshl_add_u32 v116, v8, 4, v9
	v_dot8_i32_i4 v8, v42, v1, 0
	v_dot8_i32_i4 v9, v42, v88, 0
	v_dot8_i32_i4 v8, v43, v89, v8
	v_dot8_i32_i4 v9, v43, v90, v9
	s_waitcnt lgkmcnt(0)
	v_add_u32_e32 v107, v107, v115
	v_permlane32_swap_b32 v108, v116
	v_lshl_add_u32 v117, v8, 4, v9
	v_dot8_i32_i4 v8, v40, v1, 0
	v_dot8_i32_i4 v9, v40, v88, 0
	v_dot8_i32_i4 v8, v41, v89, v8
	v_dot8_i32_i4 v9, v41, v90, v9
	s_waitcnt lgkmcnt(0)
	v_add_u32_e32 v108, v108, v116
	v_permlane32_swap_b32 v109, v117
	v_lshl_add_u32 v118, v8, 4, v9
	s_waitcnt lgkmcnt(0)
	v_add_u32_e32 v109, v109, v117
	v_permlane32_swap_b32 v110, v118
	v_readlane_b32 s50, v92, 12
	s_lshl_b64 s[16:17], s[16:17], 9
	s_ashr_i32 s19, s18, 31
	s_waitcnt lgkmcnt(0)
	v_add_u32_e32 v110, v110, v118
	v_permlane16_swap_b32 v87, v107
	v_readlane_b32 s20, v92, 4
	s_add_u32 s66, s28, s62
	s_addc_u32 s67, s29, s63
	global_load_dwordx2 v[24:25], v121, s[66:67]
	s_add_u32 s66, s30, s62
	s_addc_u32 s67, s31, s63
	global_load_dwordx2 v[38:39], v121, s[66:67]
	s_waitcnt lgkmcnt(0)
	v_add_u32_e32 v87, v87, v107
	v_permlane16_swap_b32 v104, v108
	s_lshl_b64 s[38:39], s[38:39], 9
	s_ashr_i32 s51, s50, 31
	v_readlane_b32 s52, v92, 13
	s_waitcnt lgkmcnt(0)
	v_add_u32_e32 v104, v104, v108
	v_permlane16_swap_b32 v105, v109
	s_lshl_b64 s[18:19], s[18:19], 9
	s_ashr_i32 s21, s20, 31
	v_readlane_b32 s22, v92, 5
	s_waitcnt lgkmcnt(0)
	v_add_u32_e32 v105, v105, v109
	v_permlane16_swap_b32 v106, v110
	s_add_u32 s66, s34, s62
	s_addc_u32 s67, s35, s63
	global_load_dwordx2 v[50:51], v121, s[66:67]
	s_lshl_b64 s[50:51], s[50:51], 9
	s_ashr_i32 s53, s52, 31
	s_waitcnt lgkmcnt(0)
	v_add_u32_e32 v106, v106, v110
	v_cndmask_b32_e64 v107, v87, v105, s[44:45]
	v_cndmask_b32_e64 v87, v105, v87, s[44:45]
	s_nop 0
	v_readlane_b32 s54, v92, 14
	s_lshl_b64 s[20:21], s[20:21], 9
	s_ashr_i32 s23, s22, 31
	v_readlane_b32 s24, v92, 6
	s_waitcnt lgkmcnt(0)
	v_add_u32_dpp v87, v107, v87 row_ror:8 row_mask:0xf bank_mask:0xf
	v_cndmask_b32_e64 v105, v104, v106, s[44:45]
	s_nop 1
	v_cndmask_b32_e64 v104, v106, v104, s[44:45]
	s_lshl_b64 s[52:53], s[52:53], 9
	s_ashr_i32 s55, s54, 31
	v_readlane_b32 s56, v92, 15
	s_waitcnt lgkmcnt(0)
	v_add_u32_dpp v104, v105, v104 row_ror:8 row_mask:0xf bank_mask:0xf
	v_cndmask_b32_e64 v105, v87, v104, s[46:47]
	v_cndmask_b32_e64 v87, v104, v87, s[46:47]
	s_nop 0
	v_mov_b32_dpp v104, v105 row_half_mirror row_mask:0xf bank_mask:0xf
	s_nop 1
	s_lshl_b64 s[22:23], s[22:23], 9
	s_ashr_i32 s25, s24, 31
	v_readlane_b32 s26, v92, 7
	s_lshl_b64 s[54:55], s[54:55], 9
	s_waitcnt lgkmcnt(0)
	v_add_u32_dpp v87, v104, v87 quad_perm:[3,2,1,0] row_mask:0xf bank_mask:0xf
	s_nop 1
	s_ashr_i32 s57, s56, 31
	s_lshl_b64 s[24:25], s[24:25], 9
	s_ashr_i32 s27, s26, 31
	s_lshl_b64 s[56:57], s[56:57], 9
	s_waitcnt lgkmcnt(0)
	v_add_u32_dpp v87, v87, v87 quad_perm:[2,3,0,1] row_mask:0xf bank_mask:0xf
	s_nop 1
	s_lshl_b64 s[26:27], s[26:27], 9
	s_add_u32 s66, s38, s62
	s_addc_u32 s67, s39, s63
	global_load_dwordx2 v[48:49], v121, s[66:67]
	s_add_u32 s66, s50, s62
	s_addc_u32 s67, s51, s63
	global_load_dwordx2 v[46:47], v121, s[66:67]
	s_add_u32 s66, s52, s62
	s_addc_u32 s67, s53, s63
	global_load_dwordx2 v[44:45], v121, s[66:67]
	s_add_u32 s66, s54, s62
	s_addc_u32 s67, s55, s63
	global_load_dwordx2 v[42:43], v121, s[66:67]
	s_add_u32 s66, s56, s62
	s_addc_u32 s67, s57, s63
	global_load_dwordx2 v[40:41], v121, s[66:67]
	s_add_u32 s66, s12, s62
	s_addc_u32 s67, s13, s63
	global_load_dwordx2 v[8:9], v121, s[66:67]
	s_add_u32 s66, s14, s62
	s_addc_u32 s67, s15, s63
	global_load_dwordx2 v[10:11], v121, s[66:67]
	s_add_u32 s66, s16, s62
	s_addc_u32 s67, s17, s63
	global_load_dwordx2 v[12:13], v121, s[66:67]
	s_add_u32 s66, s18, s62
	s_addc_u32 s67, s19, s63
	global_load_dwordx2 v[14:15], v121, s[66:67]
	s_add_u32 s66, s20, s62
	s_addc_u32 s67, s21, s63
	global_load_dwordx2 v[16:17], v121, s[66:67]
	s_add_u32 s66, s22, s62
	s_addc_u32 s67, s23, s63
	global_load_dwordx2 v[18:19], v121, s[66:67]
	s_add_u32 s66, s24, s62
	s_addc_u32 s67, s25, s63
	global_load_dwordx2 v[20:21], v121, s[66:67]
	s_add_u32 s66, s26, s62
	s_addc_u32 s67, s27, s63
	global_load_dwordx2 v[22:23], v121, s[66:67]
	s_waitcnt lgkmcnt(0)
	v_add_u32_dpp v87, v87, v87 quad_perm:[1,0,3,2] row_mask:0xf bank_mask:0xf
	s_waitcnt vmcnt(17)
	v_mul_f32_e32 v85, v91, v85
	v_cvt_f32_i32_e32 v87, v87
	v_add_f32_e32 v87, v95, v87
	v_mul_f32_e32 v85, v85, v87
	v_mul_f32_e32 v87, 0x3d372713, v85
	v_mul_f32_e32 v87, v85, v87
	v_fma_f32 v87, v85, v87, v85
	v_mul_f32_e32 v87, 0x3fcc422a, v87
	v_mul_f32_e32 v87, 0xbfb8aa3b, v87
	v_exp_f32_e32 v87, v87
	s_nop 0
	v_add_f32_e32 v87, 1.0, v87
	v_rcp_f32_e32 v87, v87
	s_nop 0
	v_pk_mul_f32 v[84:85], v[84:85], v[86:87]
	s_waitcnt vmcnt(34)
	v_alignbit_b32 v224, v82, v82, 4
	v_pk_mul_f32 v[84:85], v[84:85], v[84:85] op_sel:[0,1] op_sel_hi:[1,0]
	v_cvt_f16_f32_e32 v120, v84
	v_and_b32_e32 v86, 0x7070707, v82
	v_readlane_b32 s36, v120, 0
	v_and_b32_e32 v87, 0x7070707, v224
	v_perm_b32 v86, s2, v205, v86
	v_perm_b32 v87, s2, v205, v87
	v_and_or_b32 v86, v82, s4, v86
	v_and_or_b32 v82, v224, s4, v87
	v_perm_b32 v87, v82, v86, s5
	v_perm_b32 v104, v82, v86, s33
	v_perm_b32 v105, v82, v86, s0
	v_perm_b32 v82, v82, v86, s1
	v_pk_fma_f16 v86, v87, s36, v103 op_sel_hi:[1,0,1]
	v_pk_fma_f16 v87, v104, s36, v102 op_sel_hi:[1,0,1]
	v_alignbit_b32 v225, v83, v83, 4
	v_pk_fma_f16 v82, v82, s36, v100 op_sel_hi:[1,0,1]
	v_and_b32_e32 v100, 0x7070707, v83
	v_and_b32_e32 v102, 0x7070707, v225
	v_perm_b32 v100, s2, v205, v100
	v_perm_b32 v102, s2, v205, v102
	v_and_or_b32 v100, v83, s4, v100
	v_and_or_b32 v83, v225, s4, v102
	v_perm_b32 v102, v83, v100, s5
	v_perm_b32 v103, v83, v100, s33
	v_perm_b32 v104, v83, v100, s0
	v_perm_b32 v83, v83, v100, s1
	v_readlane_b32 s59, v120, 4
	s_waitcnt vmcnt(33)
	v_alignbit_b32 v224, v80, v80, 4
	v_pk_fma_f16 v101, v105, s36, v101 op_sel_hi:[1,0,1]
	v_pk_fma_f16 v99, v102, s36, v99 op_sel_hi:[1,0,1]
	v_pk_fma_f16 v98, v103, s36, v98 op_sel_hi:[1,0,1]
	v_pk_fma_f16 v97, v104, s36, v97 op_sel_hi:[1,0,1]
	v_pk_fma_f16 v83, v83, s36, v96 op_sel_hi:[1,0,1]
	s_setprio 0
	v_and_b32_e32 v96, 0x7070707, v80
	v_and_b32_e32 v100, 0x7070707, v224
	v_perm_b32 v96, s2, v205, v96
	v_perm_b32 v100, s2, v205, v100
	v_and_or_b32 v96, v80, s4, v96
	v_and_or_b32 v80, v224, s4, v100
	v_perm_b32 v100, v80, v96, s5
	v_perm_b32 v102, v80, v96, s33
	v_perm_b32 v103, v80, v96, s0
	v_perm_b32 v80, v80, v96, s1
	v_pk_fma_f16 v86, v100, s59, v86 op_sel_hi:[1,0,1]
	v_alignbit_b32 v225, v81, v81, 4
	v_pk_fma_f16 v80, v80, s59, v82 op_sel_hi:[1,0,1]
	v_and_b32_e32 v82, 0x7070707, v81
	v_and_b32_e32 v100, 0x7070707, v225
	v_pk_fma_f16 v96, v103, s59, v101 op_sel_hi:[1,0,1]
	v_perm_b32 v82, s2, v205, v82
	v_perm_b32 v100, s2, v205, v100
	v_and_or_b32 v82, v81, s4, v82
	v_and_or_b32 v81, v225, s4, v100
	v_perm_b32 v100, v81, v82, s5
	v_pk_fma_f16 v87, v102, s59, v87 op_sel_hi:[1,0,1]
	v_perm_b32 v101, v81, v82, s33
	v_perm_b32 v102, v81, v82, s0
	v_perm_b32 v81, v81, v82, s1
	v_pk_fma_f16 v82, v100, s59, v99 op_sel_hi:[1,0,1]
	v_readlane_b32 s60, v120, 8
	s_waitcnt vmcnt(32)
	v_alignbit_b32 v224, v78, v78, 4
	v_pk_fma_f16 v98, v101, s59, v98 op_sel_hi:[1,0,1]
	v_pk_fma_f16 v97, v102, s59, v97 op_sel_hi:[1,0,1]
	v_pk_fma_f16 v81, v81, s59, v83 op_sel_hi:[1,0,1]
	v_and_b32_e32 v85, 0x7070707, v78
	v_and_b32_e32 v99, 0x7070707, v224
	v_perm_b32 v85, s2, v205, v85
	v_perm_b32 v99, s2, v205, v99
	v_and_or_b32 v85, v78, s4, v85
	v_and_or_b32 v78, v224, s4, v99
	v_perm_b32 v99, v78, v85, s5
	v_perm_b32 v100, v78, v85, s33
	v_perm_b32 v101, v78, v85, s0
	v_perm_b32 v78, v78, v85, s1
	v_pk_fma_f16 v85, v99, s60, v86 op_sel_hi:[1,0,1]
	v_pk_fma_f16 v86, v100, s60, v87 op_sel_hi:[1,0,1]
	v_pk_fma_f16 v87, v101, s60, v96 op_sel_hi:[1,0,1]
	v_alignbit_b32 v225, v79, v79, 4
	v_pk_fma_f16 v78, v78, s60, v80 op_sel_hi:[1,0,1]
	v_and_b32_e32 v80, 0x7070707, v79
	v_and_b32_e32 v96, 0x7070707, v225
	v_perm_b32 v80, s2, v205, v80
	v_perm_b32 v96, s2, v205, v96
	v_and_or_b32 v80, v79, s4, v80
	v_and_or_b32 v79, v225, s4, v96
	v_perm_b32 v96, v79, v80, s5
	v_perm_b32 v100, v79, v80, s0
	v_perm_b32 v99, v79, v80, s33
	v_perm_b32 v79, v79, v80, s1
	v_pk_fma_f16 v80, v96, s60, v82 op_sel_hi:[1,0,1]
	v_pk_fma_f16 v96, v100, s60, v97 op_sel_hi:[1,0,1]
	v_readlane_b32 s36, v120, 12
	s_waitcnt vmcnt(31)
	v_alignbit_b32 v224, v76, v76, 4
	v_pk_fma_f16 v82, v99, s60, v98 op_sel_hi:[1,0,1]
	v_pk_fma_f16 v79, v79, s60, v81 op_sel_hi:[1,0,1]
	v_and_b32_e32 v83, 0x7070707, v76
	v_and_b32_e32 v97, 0x7070707, v224
	v_perm_b32 v83, s2, v205, v83
	v_perm_b32 v97, s2, v205, v97
	v_and_or_b32 v83, v76, s4, v83
	v_and_or_b32 v76, v224, s4, v97
	v_perm_b32 v97, v76, v83, s5
	v_perm_b32 v98, v76, v83, s33
	v_perm_b32 v99, v76, v83, s0
	v_perm_b32 v76, v76, v83, s1
	v_pk_fma_f16 v83, v97, s36, v85 op_sel_hi:[1,0,1]
	v_pk_fma_f16 v85, v98, s36, v86 op_sel_hi:[1,0,1]
	v_pk_fma_f16 v86, v99, s36, v87 op_sel_hi:[1,0,1]
	v_alignbit_b32 v225, v77, v77, 4
	v_pk_fma_f16 v76, v76, s36, v78 op_sel_hi:[1,0,1]
	v_and_b32_e32 v78, 0x7070707, v77
	v_and_b32_e32 v87, 0x7070707, v225
	v_perm_b32 v78, s2, v205, v78
	v_perm_b32 v87, s2, v205, v87
	v_and_or_b32 v78, v77, s4, v78
	v_and_or_b32 v77, v225, s4, v87
	v_perm_b32 v87, v77, v78, s5
	v_perm_b32 v97, v77, v78, s33
	v_perm_b32 v98, v77, v78, s0
	v_perm_b32 v77, v77, v78, s1
	v_pk_fma_f16 v78, v87, s36, v80 op_sel_hi:[1,0,1]
	v_readlane_b32 s59, v120, 16
	s_waitcnt vmcnt(30)
	v_alignbit_b32 v224, v74, v74, 4
	v_pk_fma_f16 v80, v97, s36, v82 op_sel_hi:[1,0,1]
	v_pk_fma_f16 v82, v98, s36, v96 op_sel_hi:[1,0,1]
	v_pk_fma_f16 v77, v77, s36, v79 op_sel_hi:[1,0,1]
	v_and_b32_e32 v81, 0x7070707, v74
	v_and_b32_e32 v87, 0x7070707, v224
	v_perm_b32 v81, s2, v205, v81
	v_perm_b32 v87, s2, v205, v87
	v_and_or_b32 v81, v74, s4, v81
	v_and_or_b32 v74, v224, s4, v87
	v_perm_b32 v87, v74, v81, s5
	v_perm_b32 v96, v74, v81, s33
	v_perm_b32 v97, v74, v81, s0
	v_perm_b32 v74, v74, v81, s1
	v_pk_fma_f16 v81, v87, s59, v83 op_sel_hi:[1,0,1]
	v_pk_fma_f16 v83, v96, s59, v85 op_sel_hi:[1,0,1]
	v_pk_fma_f16 v85, v97, s59, v86 op_sel_hi:[1,0,1]
	v_alignbit_b32 v225, v75, v75, 4
	v_pk_fma_f16 v74, v74, s59, v76 op_sel_hi:[1,0,1]
	v_and_b32_e32 v76, 0x7070707, v75
	v_and_b32_e32 v86, 0x7070707, v225
	v_perm_b32 v76, s2, v205, v76
	v_perm_b32 v86, s2, v205, v86
	v_and_or_b32 v76, v75, s4, v76
	v_and_or_b32 v75, v225, s4, v86
	v_perm_b32 v86, v75, v76, s5
	v_perm_b32 v87, v75, v76, s33
	v_perm_b32 v96, v75, v76, s0
	v_perm_b32 v75, v75, v76, s1
	v_pk_fma_f16 v76, v86, s59, v78 op_sel_hi:[1,0,1]
	v_pk_fma_f16 v78, v87, s59, v80 op_sel_hi:[1,0,1]
	v_pk_fma_f16 v80, v96, s59, v82 op_sel_hi:[1,0,1]
	v_readlane_b32 s60, v120, 20
	s_waitcnt vmcnt(29)
	v_alignbit_b32 v224, v70, v70, 4
	v_pk_fma_f16 v75, v75, s59, v77 op_sel_hi:[1,0,1]
	v_and_b32_e32 v79, 0x7070707, v70
	v_and_b32_e32 v82, 0x7070707, v224
	v_perm_b32 v79, s2, v205, v79
	v_perm_b32 v82, s2, v205, v82
	v_and_or_b32 v79, v70, s4, v79
	v_and_or_b32 v70, v224, s4, v82
	v_perm_b32 v82, v70, v79, s5
	v_perm_b32 v86, v70, v79, s33
	v_perm_b32 v87, v70, v79, s0
	v_perm_b32 v70, v70, v79, s1
	v_pk_fma_f16 v79, v82, s60, v81 op_sel_hi:[1,0,1]
	v_pk_fma_f16 v81, v86, s60, v83 op_sel_hi:[1,0,1]
	v_alignbit_b32 v225, v71, v71, 4
	v_pk_fma_f16 v70, v70, s60, v74 op_sel_hi:[1,0,1]
	v_and_b32_e32 v74, 0x7070707, v71
	v_and_b32_e32 v83, 0x7070707, v225
	v_pk_fma_f16 v82, v87, s60, v85 op_sel_hi:[1,0,1]
	v_perm_b32 v74, s2, v205, v74
	v_perm_b32 v83, s2, v205, v83
	v_and_or_b32 v74, v71, s4, v74
	v_and_or_b32 v71, v225, s4, v83
	v_perm_b32 v83, v71, v74, s5
	v_perm_b32 v85, v71, v74, s33
	v_perm_b32 v86, v71, v74, s0
	v_perm_b32 v71, v71, v74, s1
	v_pk_fma_f16 v74, v83, s60, v76 op_sel_hi:[1,0,1]
	v_pk_fma_f16 v76, v85, s60, v78 op_sel_hi:[1,0,1]
	v_pk_fma_f16 v78, v86, s60, v80 op_sel_hi:[1,0,1]
	v_readlane_b32 s36, v120, 24
	s_waitcnt vmcnt(28)
	v_alignbit_b32 v224, v68, v68, 4
	v_pk_fma_f16 v71, v71, s60, v75 op_sel_hi:[1,0,1]
	v_and_b32_e32 v77, 0x7070707, v68
	v_and_b32_e32 v80, 0x7070707, v224
	v_perm_b32 v77, s2, v205, v77
	v_perm_b32 v80, s2, v205, v80
	v_and_or_b32 v77, v68, s4, v77
	v_and_or_b32 v68, v224, s4, v80
	v_perm_b32 v80, v68, v77, s5
	v_perm_b32 v83, v68, v77, s33
	v_perm_b32 v85, v68, v77, s0
	v_perm_b32 v68, v68, v77, s1
	v_pk_fma_f16 v77, v80, s36, v79 op_sel_hi:[1,0,1]
	v_pk_fma_f16 v79, v83, s36, v81 op_sel_hi:[1,0,1]
	v_alignbit_b32 v225, v69, v69, 4
	v_pk_fma_f16 v68, v68, s36, v70 op_sel_hi:[1,0,1]
	v_and_b32_e32 v70, 0x7070707, v69
	v_and_b32_e32 v81, 0x7070707, v225
	v_pk_fma_f16 v80, v85, s36, v82 op_sel_hi:[1,0,1]
	v_perm_b32 v70, s2, v205, v70
	v_perm_b32 v81, s2, v205, v81
	v_and_or_b32 v70, v69, s4, v70
	v_and_or_b32 v69, v225, s4, v81
	v_perm_b32 v81, v69, v70, s5
	v_perm_b32 v82, v69, v70, s33
	v_perm_b32 v83, v69, v70, s0
	v_perm_b32 v69, v69, v70, s1
	v_pk_fma_f16 v70, v81, s36, v74 op_sel_hi:[1,0,1]
	v_pk_fma_f16 v74, v82, s36, v76 op_sel_hi:[1,0,1]
	v_pk_fma_f16 v76, v83, s36, v78 op_sel_hi:[1,0,1]
	v_readlane_b32 s59, v120, 28
	s_waitcnt vmcnt(25)
	v_alignbit_b32 v224, v64, v64, 4
	v_pk_fma_f16 v69, v69, s36, v71 op_sel_hi:[1,0,1]
	v_and_b32_e32 v75, 0x7070707, v64
	v_and_b32_e32 v78, 0x7070707, v224
	v_perm_b32 v75, s2, v205, v75
	v_perm_b32 v78, s2, v205, v78
	v_and_or_b32 v75, v64, s4, v75
	v_and_or_b32 v64, v224, s4, v78
	v_perm_b32 v78, v64, v75, s5
	v_perm_b32 v81, v64, v75, s33
	v_perm_b32 v82, v64, v75, s0
	v_perm_b32 v64, v64, v75, s1
	v_pk_fma_f16 v75, v78, s59, v77 op_sel_hi:[1,0,1]
	v_pk_fma_f16 v77, v81, s59, v79 op_sel_hi:[1,0,1]
	v_alignbit_b32 v225, v65, v65, 4
	v_pk_fma_f16 v64, v64, s59, v68 op_sel_hi:[1,0,1]
	v_and_b32_e32 v68, 0x7070707, v65
	v_and_b32_e32 v79, 0x7070707, v225
	v_pk_fma_f16 v78, v82, s59, v80 op_sel_hi:[1,0,1]
	s_add_u32 s66, s12, s64
	s_addc_u32 s67, s13, s65
	global_load_dwordx2 v[82:83], v121, s[66:67]
	v_perm_b32 v68, s2, v205, v68
	v_perm_b32 v79, s2, v205, v79
	v_and_or_b32 v68, v65, s4, v68
	v_and_or_b32 v65, v225, s4, v79
	v_perm_b32 v79, v65, v68, s5
	v_perm_b32 v80, v65, v68, s33
	v_perm_b32 v81, v65, v68, s0
	v_perm_b32 v65, v65, v68, s1
	v_pk_fma_f16 v68, v79, s59, v70 op_sel_hi:[1,0,1]
	v_pk_fma_f16 v70, v80, s59, v74 op_sel_hi:[1,0,1]
	v_pk_fma_f16 v74, v81, s59, v76 op_sel_hi:[1,0,1]
	v_readlane_b32 s60, v120, 32
	s_waitcnt vmcnt(25)
	v_alignbit_b32 v224, v62, v62, 4
	v_pk_fma_f16 v65, v65, s59, v69 op_sel_hi:[1,0,1]
	v_and_b32_e32 v71, 0x7070707, v62
	v_and_b32_e32 v76, 0x7070707, v224
	v_perm_b32 v71, s2, v205, v71
	v_perm_b32 v76, s2, v205, v76
	v_and_or_b32 v71, v62, s4, v71
	v_and_or_b32 v62, v224, s4, v76
	v_perm_b32 v76, v62, v71, s5
	v_perm_b32 v79, v62, v71, s33
	v_perm_b32 v80, v62, v71, s0
	v_perm_b32 v62, v62, v71, s1
	v_pk_fma_f16 v71, v76, s60, v75 op_sel_hi:[1,0,1]
	v_pk_fma_f16 v75, v79, s60, v77 op_sel_hi:[1,0,1]
	v_alignbit_b32 v225, v63, v63, 4
	v_pk_fma_f16 v62, v62, s60, v64 op_sel_hi:[1,0,1]
	v_and_b32_e32 v64, 0x7070707, v63
	v_and_b32_e32 v77, 0x7070707, v225
	v_pk_fma_f16 v76, v80, s60, v78 op_sel_hi:[1,0,1]
	s_add_u32 s66, s14, s64
	s_addc_u32 s67, s15, s65
	global_load_dwordx2 v[80:81], v121, s[66:67]
	v_perm_b32 v64, s2, v205, v64
	v_perm_b32 v77, s2, v205, v77
	v_and_or_b32 v64, v63, s4, v64
	v_and_or_b32 v63, v225, s4, v77
	v_perm_b32 v77, v63, v64, s5
	v_perm_b32 v78, v63, v64, s33
	v_perm_b32 v79, v63, v64, s0
	v_perm_b32 v63, v63, v64, s1
	v_pk_fma_f16 v64, v77, s60, v68 op_sel_hi:[1,0,1]
	v_pk_fma_f16 v68, v78, s60, v70 op_sel_hi:[1,0,1]
	v_pk_fma_f16 v70, v79, s60, v74 op_sel_hi:[1,0,1]
	v_readlane_b32 s36, v120, 36
	s_waitcnt vmcnt(29)
	v_alignbit_b32 v224, v66, v66, 4
	v_pk_fma_f16 v63, v63, s60, v65 op_sel_hi:[1,0,1]
	v_and_b32_e32 v69, 0x7070707, v66
	v_and_b32_e32 v74, 0x7070707, v224
	v_perm_b32 v69, s2, v205, v69
	v_perm_b32 v74, s2, v205, v74
	v_and_or_b32 v69, v66, s4, v69
	v_and_or_b32 v66, v224, s4, v74
	v_perm_b32 v74, v66, v69, s5
	v_perm_b32 v77, v66, v69, s33
	v_perm_b32 v78, v66, v69, s0
	v_perm_b32 v66, v66, v69, s1
	v_pk_fma_f16 v69, v74, s36, v71 op_sel_hi:[1,0,1]
	v_pk_fma_f16 v71, v77, s36, v75 op_sel_hi:[1,0,1]
	v_alignbit_b32 v225, v67, v67, 4
	v_pk_fma_f16 v62, v66, s36, v62 op_sel_hi:[1,0,1]
	v_and_b32_e32 v66, 0x7070707, v67
	v_and_b32_e32 v75, 0x7070707, v225
	v_pk_fma_f16 v74, v78, s36, v76 op_sel_hi:[1,0,1]
	s_add_u32 s66, s16, s64
	s_addc_u32 s67, s17, s65
	global_load_dwordx2 v[78:79], v121, s[66:67]
	v_perm_b32 v66, s2, v205, v66
	v_perm_b32 v75, s2, v205, v75
	v_and_or_b32 v66, v67, s4, v66
	v_and_or_b32 v67, v225, s4, v75
	v_perm_b32 v76, v67, v66, s33
	v_perm_b32 v77, v67, v66, s0
	v_perm_b32 v75, v67, v66, s5
	v_perm_b32 v66, v67, v66, s1
	v_pk_fma_f16 v67, v76, s36, v68 op_sel_hi:[1,0,1]
	v_pk_fma_f16 v68, v77, s36, v70 op_sel_hi:[1,0,1]
	v_readlane_b32 s59, v120, 40
	s_waitcnt vmcnt(26)
	v_alignbit_b32 v224, v60, v60, 4
	v_pk_fma_f16 v64, v75, s36, v64 op_sel_hi:[1,0,1]
	v_pk_fma_f16 v63, v66, s36, v63 op_sel_hi:[1,0,1]
	v_and_b32_e32 v66, 0x7070707, v60
	v_and_b32_e32 v70, 0x7070707, v224
	v_perm_b32 v66, s2, v205, v66
	v_perm_b32 v70, s2, v205, v70
	v_and_or_b32 v66, v60, s4, v66
	v_and_or_b32 v60, v224, s4, v70
	v_perm_b32 v70, v60, v66, s5
	v_perm_b32 v75, v60, v66, s33
	v_perm_b32 v76, v60, v66, s0
	v_perm_b32 v60, v60, v66, s1
	v_pk_fma_f16 v66, v70, s59, v69 op_sel_hi:[1,0,1]
	v_pk_fma_f16 v69, v75, s59, v71 op_sel_hi:[1,0,1]
	v_alignbit_b32 v225, v61, v61, 4
	v_pk_fma_f16 v60, v60, s59, v62 op_sel_hi:[1,0,1]
	v_and_b32_e32 v62, 0x7070707, v61
	v_and_b32_e32 v71, 0x7070707, v225
	v_pk_fma_f16 v70, v76, s59, v74 op_sel_hi:[1,0,1]
	s_add_u32 s66, s18, s64
	s_addc_u32 s67, s19, s65
	global_load_dwordx2 v[76:77], v121, s[66:67]
	v_perm_b32 v62, s2, v205, v62
	v_perm_b32 v71, s2, v205, v71
	v_and_or_b32 v62, v61, s4, v62
	v_and_or_b32 v61, v225, s4, v71
	v_perm_b32 v71, v61, v62, s5
	v_perm_b32 v74, v61, v62, s33
	v_perm_b32 v75, v61, v62, s0
	v_perm_b32 v61, v61, v62, s1
	v_pk_fma_f16 v62, v71, s59, v64 op_sel_hi:[1,0,1]
	v_pk_fma_f16 v64, v74, s59, v67 op_sel_hi:[1,0,1]
	v_pk_fma_f16 v67, v75, s59, v68 op_sel_hi:[1,0,1]
	v_readlane_b32 s60, v120, 44
	s_waitcnt vmcnt(26)
	v_alignbit_b32 v224, v58, v58, 4
	v_pk_fma_f16 v61, v61, s59, v63 op_sel_hi:[1,0,1]
	v_and_b32_e32 v65, 0x7070707, v58
	v_and_b32_e32 v68, 0x7070707, v224
	v_perm_b32 v65, s2, v205, v65
	v_perm_b32 v68, s2, v205, v68
	v_and_or_b32 v65, v58, s4, v65
	v_and_or_b32 v58, v224, s4, v68
	v_perm_b32 v68, v58, v65, s5
	v_perm_b32 v71, v58, v65, s33
	v_perm_b32 v74, v58, v65, s0
	v_perm_b32 v58, v58, v65, s1
	v_pk_fma_f16 v65, v68, s60, v66 op_sel_hi:[1,0,1]
	v_pk_fma_f16 v66, v71, s60, v69 op_sel_hi:[1,0,1]
	v_alignbit_b32 v225, v59, v59, 4
	v_pk_fma_f16 v58, v58, s60, v60 op_sel_hi:[1,0,1]
	v_and_b32_e32 v60, 0x7070707, v59
	v_and_b32_e32 v69, 0x7070707, v225
	v_pk_fma_f16 v68, v74, s60, v70 op_sel_hi:[1,0,1]
	s_add_u32 s66, s20, s64
	s_addc_u32 s67, s21, s65
	global_load_dwordx2 v[74:75], v121, s[66:67]
	v_perm_b32 v60, s2, v205, v60
	v_perm_b32 v69, s2, v205, v69
	v_and_or_b32 v60, v59, s4, v60
	v_and_or_b32 v59, v225, s4, v69
	v_perm_b32 v69, v59, v60, s5
	v_perm_b32 v70, v59, v60, s33
	v_perm_b32 v71, v59, v60, s0
	v_perm_b32 v59, v59, v60, s1
	v_pk_fma_f16 v60, v69, s60, v62 op_sel_hi:[1,0,1]
	v_pk_fma_f16 v62, v70, s60, v64 op_sel_hi:[1,0,1]
	v_pk_fma_f16 v64, v71, s60, v67 op_sel_hi:[1,0,1]
	v_readlane_b32 s36, v120, 48
	s_waitcnt vmcnt(26)
	v_alignbit_b32 v224, v56, v56, 4
	v_pk_fma_f16 v59, v59, s60, v61 op_sel_hi:[1,0,1]
	v_and_b32_e32 v63, 0x7070707, v56
	v_and_b32_e32 v67, 0x7070707, v224
	v_perm_b32 v63, s2, v205, v63
	v_perm_b32 v67, s2, v205, v67
	v_and_or_b32 v63, v56, s4, v63
	v_and_or_b32 v56, v224, s4, v67
	v_perm_b32 v67, v56, v63, s5
	v_perm_b32 v69, v56, v63, s33
	v_perm_b32 v70, v56, v63, s0
	v_perm_b32 v56, v56, v63, s1
	v_pk_fma_f16 v63, v67, s36, v65 op_sel_hi:[1,0,1]
	v_alignbit_b32 v225, v57, v57, 4
	v_pk_fma_f16 v56, v56, s36, v58 op_sel_hi:[1,0,1]
	v_and_b32_e32 v58, 0x7070707, v57
	v_and_b32_e32 v67, 0x7070707, v225
	v_pk_fma_f16 v65, v69, s36, v66 op_sel_hi:[1,0,1]
	v_pk_fma_f16 v66, v70, s36, v68 op_sel_hi:[1,0,1]
	s_add_u32 s66, s22, s64
	s_addc_u32 s67, s23, s65
	global_load_dwordx2 v[70:71], v121, s[66:67]
	v_perm_b32 v58, s2, v205, v58
	v_perm_b32 v67, s2, v205, v67
	v_and_or_b32 v58, v57, s4, v58
	v_and_or_b32 v57, v225, s4, v67
	v_perm_b32 v67, v57, v58, s5
	v_perm_b32 v68, v57, v58, s33
	v_perm_b32 v69, v57, v58, s0
	v_perm_b32 v57, v57, v58, s1
	v_pk_fma_f16 v58, v67, s36, v60 op_sel_hi:[1,0,1]
	v_pk_fma_f16 v60, v68, s36, v62 op_sel_hi:[1,0,1]
	v_pk_fma_f16 v62, v69, s36, v64 op_sel_hi:[1,0,1]
	v_readlane_b32 s59, v120, 52
	s_waitcnt vmcnt(26)
	v_alignbit_b32 v224, v54, v54, 4
	v_pk_fma_f16 v57, v57, s36, v59 op_sel_hi:[1,0,1]
	v_and_b32_e32 v61, 0x7070707, v54
	v_and_b32_e32 v64, 0x7070707, v224
	v_perm_b32 v61, s2, v205, v61
	v_perm_b32 v64, s2, v205, v64
	v_and_or_b32 v61, v54, s4, v61
	v_and_or_b32 v54, v224, s4, v64
	v_perm_b32 v64, v54, v61, s5
	v_perm_b32 v67, v54, v61, s33
	v_perm_b32 v68, v54, v61, s0
	v_perm_b32 v54, v54, v61, s1
	v_pk_fma_f16 v61, v64, s59, v63 op_sel_hi:[1,0,1]
	v_pk_fma_f16 v63, v67, s59, v65 op_sel_hi:[1,0,1]
	v_alignbit_b32 v225, v55, v55, 4
	v_pk_fma_f16 v54, v54, s59, v56 op_sel_hi:[1,0,1]
	v_and_b32_e32 v56, 0x7070707, v55
	v_and_b32_e32 v65, 0x7070707, v225
	v_pk_fma_f16 v64, v68, s59, v66 op_sel_hi:[1,0,1]
	s_add_u32 s66, s24, s64
	s_addc_u32 s67, s25, s65
	global_load_dwordx2 v[68:69], v121, s[66:67]
	v_perm_b32 v56, s2, v205, v56
	v_perm_b32 v65, s2, v205, v65
	v_and_or_b32 v56, v55, s4, v56
	v_and_or_b32 v55, v225, s4, v65
	v_perm_b32 v65, v55, v56, s5
	v_perm_b32 v66, v55, v56, s33
	v_perm_b32 v67, v55, v56, s0
	v_perm_b32 v55, v55, v56, s1
	v_pk_fma_f16 v56, v65, s59, v58 op_sel_hi:[1,0,1]
	v_pk_fma_f16 v58, v66, s59, v60 op_sel_hi:[1,0,1]
	v_pk_fma_f16 v60, v67, s59, v62 op_sel_hi:[1,0,1]
	v_readlane_b32 s60, v120, 56
	s_waitcnt vmcnt(26)
	v_alignbit_b32 v224, v52, v52, 4
	v_pk_fma_f16 v55, v55, s59, v57 op_sel_hi:[1,0,1]
	v_and_b32_e32 v59, 0x7070707, v52
	v_and_b32_e32 v62, 0x7070707, v224
	v_perm_b32 v59, s2, v205, v59
	v_perm_b32 v62, s2, v205, v62
	v_and_or_b32 v59, v52, s4, v59
	v_and_or_b32 v52, v224, s4, v62
	v_perm_b32 v62, v52, v59, s5
	v_perm_b32 v65, v52, v59, s33
	v_perm_b32 v66, v52, v59, s0
	v_perm_b32 v52, v52, v59, s1
	v_pk_fma_f16 v59, v62, s60, v61 op_sel_hi:[1,0,1]
	v_pk_fma_f16 v61, v65, s60, v63 op_sel_hi:[1,0,1]
	v_alignbit_b32 v225, v53, v53, 4
	v_pk_fma_f16 v52, v52, s60, v54 op_sel_hi:[1,0,1]
	v_and_b32_e32 v54, 0x7070707, v53
	v_and_b32_e32 v63, 0x7070707, v225
	v_pk_fma_f16 v62, v66, s60, v64 op_sel_hi:[1,0,1]
	s_add_u32 s66, s30, s64
	s_addc_u32 s67, s31, s65
	global_load_dwordx2 v[66:67], v121, s[66:67]
	v_perm_b32 v54, s2, v205, v54
	v_perm_b32 v63, s2, v205, v63
	v_and_or_b32 v54, v53, s4, v54
	v_and_or_b32 v53, v225, s4, v63
	v_perm_b32 v63, v53, v54, s5
	v_perm_b32 v64, v53, v54, s33
	v_perm_b32 v65, v53, v54, s0
	v_perm_b32 v53, v53, v54, s1
	v_pk_fma_f16 v54, v63, s60, v56 op_sel_hi:[1,0,1]
	v_pk_fma_f16 v56, v64, s60, v58 op_sel_hi:[1,0,1]
	v_pk_fma_f16 v58, v65, s60, v60 op_sel_hi:[1,0,1]
	v_readlane_b32 s36, v120, 60
	s_waitcnt vmcnt(34)
	v_alignbit_b32 v224, v36, v36, 4
	v_pk_fma_f16 v53, v53, s60, v55 op_sel_hi:[1,0,1]
	v_and_b32_e32 v57, 0x7070707, v36
	v_and_b32_e32 v60, 0x7070707, v224
	v_perm_b32 v57, s2, v205, v57
	v_perm_b32 v60, s2, v205, v60
	v_and_or_b32 v57, v36, s4, v57
	v_and_or_b32 v36, v224, s4, v60
	v_perm_b32 v60, v36, v57, s5
	v_perm_b32 v63, v36, v57, s33
	v_perm_b32 v64, v36, v57, s0
	v_perm_b32 v36, v36, v57, s1
	v_pk_fma_f16 v100, v36, s36, v52 op_sel_hi:[1,0,1]
	v_alignbit_b32 v225, v37, v37, 4
	v_and_b32_e32 v36, 0x7070707, v37
	v_and_b32_e32 v52, 0x7070707, v225
	v_perm_b32 v36, s2, v205, v36
	v_perm_b32 v52, s2, v205, v52
	v_and_or_b32 v36, v37, s4, v36
	v_and_or_b32 v37, v225, s4, v52
	v_pk_fma_f16 v103, v60, s36, v59 op_sel_hi:[1,0,1]
	v_perm_b32 v52, v37, v36, s5
	v_perm_b32 v57, v37, v36, s33
	v_perm_b32 v59, v37, v36, s0
	v_perm_b32 v36, v37, v36, s1
	v_pk_fma_f16 v96, v36, s36, v53 op_sel_hi:[1,0,1]
	s_add_u32 s66, s56, s64
	s_addc_u32 s67, s57, s65
	global_load_dwordx2 v[36:37], v121, s[66:67]
	v_pk_fma_f16 v101, v64, s36, v62 op_sel_hi:[1,0,1]
	s_add_u32 s66, s26, s64
	s_addc_u32 s67, s27, s65
	global_load_dwordx2 v[64:65], v121, s[66:67]
	v_pk_fma_f16 v102, v63, s36, v61 op_sel_hi:[1,0,1]
	s_add_u32 s66, s28, s64
	s_addc_u32 s67, s29, s65
	global_load_dwordx2 v[62:63], v121, s[66:67]
	s_add_u32 s66, s34, s64
	s_addc_u32 s67, s35, s65
	global_load_dwordx2 v[60:61], v121, s[66:67]
	v_pk_fma_f16 v97, v59, s36, v58 op_sel_hi:[1,0,1]
	s_add_u32 s66, s38, s64
	s_addc_u32 s67, s39, s65
	global_load_dwordx2 v[58:59], v121, s[66:67]
	v_pk_fma_f16 v98, v57, s36, v56 op_sel_hi:[1,0,1]
	s_add_u32 s66, s50, s64
	s_addc_u32 s67, s51, s65
	global_load_dwordx2 v[56:57], v121, s[66:67]
	v_pk_fma_f16 v99, v52, s36, v54 op_sel_hi:[1,0,1]
	s_add_u32 s66, s52, s64
	s_addc_u32 s67, s53, s65
	global_load_dwordx2 v[54:55], v121, s[66:67]
	s_add_u32 s66, s54, s64
	s_addc_u32 s67, s55, s65
	global_load_dwordx2 v[52:53], v121, s[66:67]
	s_nop 0
	s_nop 0
	s_nop 0
	s_nop 0
	s_nop 0
	s_nop 0
	s_nop 0
	s_cmpk_eq_i32 s58, 0x90
	s_cbranch_scc0 .LBB0_763
	v_lshlrev_b64 v[0:1], 2, v[2:3]
	v_lshl_add_u64 v[2:3], v[28:29], 0, v[0:1]
	v_mov_b32_e32 v104, v208
	v_mov_b32_e32 v105, v209
	v_mov_b32_e32 v106, v210
	v_mov_b32_e32 v107, v211
	v_mov_b32_e32 v108, v212
	v_mov_b32_e32 v109, v213
	v_mov_b32_e32 v110, v214
	v_mov_b32_e32 v111, v215
	v_mov_b32_e32 v86, v216
	v_mov_b32_e32 v87, v217
	v_mov_b32_e32 v88, v218
	v_mov_b32_e32 v89, v219
	v_mov_b32_e32 v112, v220
	v_mov_b32_e32 v113, v221
	v_mov_b32_e32 v114, v222
	v_mov_b32_e32 v115, v223
	v_lshl_add_u64 v[72:73], v[32:33], 0, v[0:1]
	v_cvt_f32_f16_sdwa v1, v103 dst_sel:DWORD dst_unused:UNUSED_PAD src0_sel:WORD_1
	v_cvt_f32_f16_e32 v0, v103
	v_cvt_f32_f16_sdwa v91, v102 dst_sel:DWORD dst_unused:UNUSED_PAD src0_sel:WORD_1
	v_cvt_f32_f16_e32 v90, v102
	v_cvt_f32_f16_sdwa v103, v101 dst_sel:DWORD dst_unused:UNUSED_PAD src0_sel:WORD_1
	v_cvt_f32_f16_e32 v102, v101
	v_cvt_f32_f16_sdwa v101, v100 dst_sel:DWORD dst_unused:UNUSED_PAD src0_sel:WORD_1
	v_cvt_f32_f16_e32 v100, v100
	s_mov_b32 s18, 0x800000
	v_readlane_b32 s12, v255, 5
	v_readlane_b32 s13, v255, 6
	v_pk_add_f32 v[86:87], v[86:87], v[102:103]
	v_pk_add_f32 v[84:85], v[112:113], v[0:1]
	v_mov_b32_e32 v102, v85
	v_mov_b32_e32 v103, v87
	v_pk_add_f32 v[90:91], v[114:115], v[90:91]
	v_pk_add_f32 v[88:89], v[88:89], v[100:101]
	v_mov_b32_e32 v100, v84
	v_mov_b32_e32 v101, v86
	v_pk_mul_f32 v[102:103], v[102:103], v[102:103]
	v_mov_b32_e32 v112, v91
	v_pk_fma_f32 v[100:101], v[100:101], v[100:101], v[102:103]
	v_mov_b32_e32 v102, v90
	v_mov_b32_e32 v103, v88
	v_pk_fma_f32 v[100:101], v[102:103], v[102:103], v[100:101]
	v_cvt_f32_f16_sdwa v103, v99 dst_sel:DWORD dst_unused:UNUSED_PAD src0_sel:WORD_1
	v_cvt_f32_f16_e32 v102, v99
	v_cvt_f32_f16_sdwa v99, v98 dst_sel:DWORD dst_unused:UNUSED_PAD src0_sel:WORD_1
	v_cvt_f32_f16_e32 v98, v98
	v_mov_b32_e32 v113, v89
	v_pk_add_f32 v[102:103], v[108:109], v[102:103]
	v_cvt_f32_f16_sdwa v109, v97 dst_sel:DWORD dst_unused:UNUSED_PAD src0_sel:WORD_1
	v_cvt_f32_f16_e32 v108, v97
	v_cvt_f32_f16_sdwa v97, v96 dst_sel:DWORD dst_unused:UNUSED_PAD src0_sel:WORD_1
	v_cvt_f32_f16_e32 v96, v96
	v_pk_add_f32 v[98:99], v[110:111], v[98:99]
	v_pk_add_f32 v[104:105], v[104:105], v[108:109]
	v_mov_b32_e32 v108, v103
	v_mov_b32_e32 v109, v105
	v_pk_add_f32 v[96:97], v[106:107], v[96:97]
	v_mov_b32_e32 v106, v102
	v_mov_b32_e32 v107, v104
	v_pk_mul_f32 v[108:109], v[108:109], v[108:109]
	v_pk_fma_f32 v[100:101], v[112:113], v[112:113], v[100:101]
	v_pk_fma_f32 v[106:107], v[106:107], v[106:107], v[108:109]
	v_mov_b32_e32 v108, v98
	v_mov_b32_e32 v109, v96
	v_mov_b32_e32 v110, v99
	v_mov_b32_e32 v111, v97
	v_pk_fma_f32 v[106:107], v[108:109], v[108:109], v[106:107]
	v_add_f32_e32 v95, v100, v101
	v_pk_fma_f32 v[106:107], v[110:111], v[110:111], v[106:107]
	v_lshl_add_u64 v[34:35], v[34:35], 0, s[12:13]
	v_add_f32_e32 v95, v95, v106
	v_add_f32_e32 v95, v95, v107
	v_mov_b32_e32 v100, v95
	s_nop 1
	v_permlane32_swap_b32 v100, v95
	s_waitcnt lgkmcnt(0)
	v_add_f32_e32 v95, v95, v100
	v_mov_b32_e32 v100, v95
	s_nop 1
	v_permlane16_swap_b32 v100, v95
	s_waitcnt lgkmcnt(0)
	v_add_f32_e32 v95, v95, v100
	s_nop 1
	v_mov_b32_dpp v100, v95 row_ror:8 row_mask:0xf bank_mask:0xf
	s_waitcnt lgkmcnt(0)
	v_add_f32_e32 v95, v95, v100
	s_nop 1
	v_mov_b32_dpp v100, v95 row_half_mirror row_mask:0xf bank_mask:0xf
	s_nop 1
	v_mov_b32_dpp v100, v100 quad_perm:[3,2,1,0] row_mask:0xf bank_mask:0xf
	s_waitcnt lgkmcnt(0)
	v_add_f32_e32 v95, v95, v100
	s_nop 1
	v_mov_b32_dpp v100, v95 quad_perm:[2,3,0,1] row_mask:0xf bank_mask:0xf
	s_waitcnt lgkmcnt(0)
	v_add_f32_e32 v95, v95, v100
	s_nop 1
	v_mov_b32_dpp v100, v95 quad_perm:[1,0,3,2] row_mask:0xf bank_mask:0xf
	s_waitcnt lgkmcnt(0)
	v_add_f32_e32 v95, v95, v100
	v_fmamk_f32 v95, v95, 0x3a800000, v191
	v_cmp_gt_f32_e32 vcc, s18, v95
	v_mul_f32_e32 v100, 0x4b800000, v95
	s_nop 0
	v_cndmask_b32_e32 v95, v95, v100, vcc
	v_rsq_f32_e32 v95, v95
	s_nop 0
	v_mul_f32_e32 v100, 0x45800000, v95
	v_cndmask_b32_e32 v100, v95, v100, vcc
	v_pk_mul_f32 v[84:85], v[84:85], v[100:101] op_sel_hi:[1,0]
	v_pk_mul_f32 v[0:1], v[124:125], v[84:85]
	v_pk_mul_f32 v[84:85], v[90:91], v[100:101] op_sel_hi:[1,0]
	s_nop 0
	v_pk_mul_f32 v[2:3], v[126:127], v[84:85]
	global_store_dwordx4 v[72:73], v[0:3], off
	s_nop 1
	v_pk_mul_f32 v[84:85], v[86:87], v[100:101] op_sel_hi:[1,0]
	v_pk_mul_f32 v[0:1], v[128:129], v[84:85]
	v_pk_mul_f32 v[84:85], v[88:89], v[100:101] op_sel_hi:[1,0]
	s_nop 0
	v_pk_mul_f32 v[2:3], v[130:131], v[84:85]
	global_store_dwordx4 v[72:73], v[0:3], off offset:16
	s_nop 1
	v_pk_mul_f32 v[84:85], v[102:103], v[100:101] op_sel_hi:[1,0]
	v_pk_mul_f32 v[0:1], v[84:85], v[132:133]
	v_pk_mul_f32 v[84:85], v[98:99], v[100:101] op_sel_hi:[1,0]
	s_nop 0
	v_pk_mul_f32 v[2:3], v[84:85], v[134:135]
	global_store_dwordx4 v[72:73], v[0:3], off offset:32
	s_nop 1
	v_pk_mul_f32 v[84:85], v[104:105], v[100:101] op_sel_hi:[1,0]
	v_pk_mul_f32 v[0:1], v[84:85], v[136:137]
	v_pk_mul_f32 v[84:85], v[96:97], v[100:101] op_sel_hi:[1,0]
	s_nop 0
	v_pk_mul_f32 v[2:3], v[84:85], v[138:139]
	global_store_dwordx4 v[72:73], v[0:3], off offset:48
	s_nop 1
	v_mov_b32_e32 v0, v94
	s_andn2_b64 exec, exec, s[10:11]
	s_cbranch_execnz .LBB0_762

.LBB0_770:
	s_cmpk_ge_i32 s56, 0x70
	s_cselect_b64 s[10:11], -1, 0
	ds_bpermute_b32 v6, v97, v96
	s_and_b64 vcc, s[10:11], s[48:49]
	v_cndmask_b32_e32 v94, v0, v98, vcc
	v_ashrrev_i32_e32 v95, 31, v94
	s_add_i32 s10, s56, 16
	s_and_b32 s10, s10, 0x70
	v_lshlrev_b64 v[94:95], 9, v[94:95]
	v_lshl_add_u64 v[94:95], s[94:95], 0, v[94:95]
	s_lshl_b32 s36, s10, 2
	s_waitcnt lgkmcnt(0)
	s_waitcnt vmcnt(32)
	v_mov_b32_e32 v96, v122
	v_ashrrev_i32_e32 v7, 31, v6
	v_lshl_add_u64 v[94:95], v[94:95], 0, s[36:37]
	v_lshl_add_u64 v[6:7], v[6:7], 3, s[88:89]
	v_lshl_add_u64 v[94:95], v[94:95], 0, v[144:145]
	global_load_dwordx2 v[6:7], v[6:7], off
	s_nop 0
	global_load_dword v8, v[4:5], off
	global_load_dword v122, v[94:95], off
	s_waitcnt vmcnt(19)
	v_dot8_i32_i4 v9, v20, v1, 0
	v_dot8_i32_i4 v94, v20, v10, 0
	v_dot8_i32_i4 v9, v21, v11, v9
	v_dot8_i32_i4 v94, v21, v12, v94
	v_dot8_i32_i4 v20, v22, v1, 0
	v_dot8_i32_i4 v21, v22, v10, 0
	v_dot8_i32_i4 v20, v23, v11, v20
	v_dot8_i32_i4 v21, v23, v12, v21
	v_lshl_add_u32 v9, v9, 4, v94
	s_add_i32 s56, s56, 16
	s_nop 0
	v_lshl_add_u32 v94, v20, 4, v21
	s_waitcnt vmcnt(19)
	v_dot8_i32_i4 v20, v24, v1, 0
	v_dot8_i32_i4 v21, v24, v10, 0
	v_dot8_i32_i4 v20, v25, v11, v20
	v_dot8_i32_i4 v21, v25, v12, v21
	v_lshl_add_u64 v[4:5], v[4:5], 0, 64
	s_nop 1
	v_lshl_add_u32 v95, v20, 4, v21
	v_dot8_i32_i4 v20, v26, v1, 0
	v_dot8_i32_i4 v21, v26, v10, 0
	v_dot8_i32_i4 v20, v27, v11, v20
	v_dot8_i32_i4 v21, v27, v12, v21
	v_readlane_b32 s10, v96, 0
	s_ashr_i32 s11, s10, 31
	v_readlane_b32 s12, v96, 1
	v_lshl_add_u32 v106, v20, 4, v21
	v_dot8_i32_i4 v20, v28, v1, 0
	v_dot8_i32_i4 v21, v28, v10, 0
	v_dot8_i32_i4 v20, v29, v11, v20
	v_dot8_i32_i4 v21, v29, v12, v21
	s_lshl_b64 s[10:11], s[10:11], 9
	s_ashr_i32 s13, s12, 31
	v_readlane_b32 s14, v96, 2
	v_lshl_add_u32 v107, v20, 4, v21
	v_dot8_i32_i4 v20, v30, v1, 0
	v_dot8_i32_i4 v21, v30, v10, 0
	v_dot8_i32_i4 v20, v31, v11, v20
	v_dot8_i32_i4 v21, v31, v12, v21
	s_lshl_b64 s[12:13], s[12:13], 9
	s_ashr_i32 s15, s14, 31
	v_readlane_b32 s16, v96, 3
	v_lshl_add_u32 v108, v20, 4, v21
	v_dot8_i32_i4 v20, v32, v1, 0
	v_dot8_i32_i4 v21, v32, v10, 0
	v_dot8_i32_i4 v20, v33, v11, v20
	v_dot8_i32_i4 v21, v33, v12, v21
	s_lshl_b64 s[14:15], s[14:15], 9
	s_ashr_i32 s17, s16, 31
	s_nop 0
	v_lshl_add_u32 v109, v20, 4, v21
	v_dot8_i32_i4 v20, v34, v1, 0
	v_dot8_i32_i4 v21, v34, v10, 0
	v_dot8_i32_i4 v20, v35, v11, v20
	v_dot8_i32_i4 v21, v35, v12, v21
	v_readlane_b32 s18, v96, 4
	s_add_u32 s66, s12, s62
	s_addc_u32 s67, s13, s63
	global_load_dwordx2 v[22:23], v121, s[66:67]
	v_lshl_add_u32 v110, v20, 4, v21
	v_dot8_i32_i4 v20, v36, v1, 0
	v_dot8_i32_i4 v21, v36, v10, 0
	v_dot8_i32_i4 v20, v37, v11, v20
	v_dot8_i32_i4 v21, v37, v12, v21
	s_lshl_b64 s[16:17], s[16:17], 9
	s_ashr_i32 s19, s18, 31
	v_readlane_b32 s20, v96, 5
	v_lshl_add_u32 v111, v20, 4, v21
	v_dot8_i32_i4 v20, v38, v1, 0
	v_dot8_i32_i4 v21, v38, v10, 0
	v_dot8_i32_i4 v20, v39, v11, v20
	v_dot8_i32_i4 v21, v39, v12, v21
	s_setprio 2
	v_permlane32_swap_b32 v9, v111
	s_nop 1
	v_lshl_add_u32 v112, v20, 4, v21
	v_dot8_i32_i4 v20, v40, v1, 0
	v_dot8_i32_i4 v21, v40, v10, 0
	v_dot8_i32_i4 v20, v41, v11, v20
	v_dot8_i32_i4 v21, v41, v12, v21
	s_waitcnt lgkmcnt(0)
	v_add_u32_e32 v9, v9, v111
	v_permlane32_swap_b32 v94, v112
	v_lshl_add_u32 v113, v20, 4, v21
	v_dot8_i32_i4 v20, v60, v1, 0
	v_dot8_i32_i4 v21, v60, v10, 0
	v_dot8_i32_i4 v20, v61, v11, v20
	v_dot8_i32_i4 v21, v61, v12, v21
	s_waitcnt lgkmcnt(0)
	v_add_u32_e32 v94, v94, v112
	v_permlane32_swap_b32 v95, v113
	v_lshl_add_u32 v114, v20, 4, v21
	v_dot8_i32_i4 v20, v58, v1, 0
	v_dot8_i32_i4 v21, v58, v10, 0
	v_dot8_i32_i4 v20, v59, v11, v20
	v_dot8_i32_i4 v21, v59, v12, v21
	s_waitcnt lgkmcnt(0)
	v_add_u32_e32 v95, v95, v113
	v_permlane32_swap_b32 v106, v114
	v_lshl_add_u32 v115, v20, 4, v21
	v_dot8_i32_i4 v20, v56, v1, 0
	v_dot8_i32_i4 v21, v56, v10, 0
	v_dot8_i32_i4 v20, v57, v11, v20
	v_dot8_i32_i4 v21, v57, v12, v21
	s_waitcnt lgkmcnt(0)
	v_add_u32_e32 v106, v106, v114
	v_permlane32_swap_b32 v107, v115
	v_lshl_add_u32 v116, v20, 4, v21
	v_dot8_i32_i4 v20, v54, v1, 0
	v_dot8_i32_i4 v21, v54, v10, 0
	v_dot8_i32_i4 v20, v55, v11, v20
	v_dot8_i32_i4 v21, v55, v12, v21
	s_waitcnt lgkmcnt(0)
	v_add_u32_e32 v107, v107, v115
	v_permlane32_swap_b32 v108, v116
	v_lshl_add_u32 v117, v20, 4, v21
	v_dot8_i32_i4 v20, v52, v1, 0
	v_dot8_i32_i4 v21, v52, v10, 0
	v_dot8_i32_i4 v20, v53, v11, v20
	v_dot8_i32_i4 v21, v53, v12, v21
	s_waitcnt lgkmcnt(0)
	v_add_u32_e32 v108, v108, v116
	v_permlane32_swap_b32 v109, v117
	v_lshl_add_u32 v118, v20, 4, v21
	s_waitcnt lgkmcnt(0)
	v_add_u32_e32 v109, v109, v117
	v_permlane32_swap_b32 v110, v118
	s_add_u32 s66, s10, s62
	s_addc_u32 s67, s11, s63
	global_load_dwordx2 v[20:21], v121, s[66:67]
	s_add_u32 s66, s14, s62
	s_addc_u32 s67, s15, s63
	global_load_dwordx2 v[24:25], v121, s[66:67]
	s_waitcnt lgkmcnt(0)
	v_add_u32_e32 v110, v110, v118
	v_permlane16_swap_b32 v9, v107
	s_lshl_b64 s[18:19], s[18:19], 9
	s_ashr_i32 s21, s20, 31
	v_readlane_b32 s22, v96, 6
	s_add_u32 s66, s16, s62
	s_addc_u32 s67, s17, s63
	global_load_dwordx2 v[26:27], v121, s[66:67]
	s_waitcnt lgkmcnt(0)
	v_add_u32_e32 v9, v9, v107
	v_permlane16_swap_b32 v94, v108
	s_lshl_b64 s[20:21], s[20:21], 9
	s_ashr_i32 s23, s22, 31
	s_waitcnt lgkmcnt(0)
	v_add_u32_e32 v94, v94, v108
	v_permlane16_swap_b32 v95, v109
	v_readlane_b32 s24, v96, 7
	s_add_u32 s66, s18, s62
	s_addc_u32 s67, s19, s63
	global_load_dwordx2 v[28:29], v121, s[66:67]
	s_waitcnt lgkmcnt(0)
	v_add_u32_e32 v95, v95, v109
	v_permlane16_swap_b32 v106, v110
	s_lshl_b64 s[22:23], s[22:23], 9
	s_ashr_i32 s25, s24, 31
	v_readlane_b32 s26, v96, 8
	s_waitcnt lgkmcnt(0)
	v_add_u32_e32 v106, v106, v110
	v_cndmask_b32_e64 v107, v9, v95, s[44:45]
	v_cndmask_b32_e64 v9, v95, v9, s[44:45]
	s_nop 0
	s_add_u32 s66, s20, s62
	s_addc_u32 s67, s21, s63
	global_load_dwordx2 v[30:31], v121, s[66:67]
	s_lshl_b64 s[24:25], s[24:25], 9
	s_ashr_i32 s27, s26, 31
	s_waitcnt lgkmcnt(0)
	v_add_u32_dpp v9, v107, v9 row_ror:8 row_mask:0xf bank_mask:0xf
	v_cndmask_b32_e64 v95, v94, v106, s[44:45]
	s_nop 1
	v_cndmask_b32_e64 v94, v106, v94, s[44:45]
	v_readlane_b32 s28, v96, 9
	s_add_u32 s66, s22, s62
	s_addc_u32 s67, s23, s63
	global_load_dwordx2 v[32:33], v121, s[66:67]
	s_waitcnt lgkmcnt(0)
	v_add_u32_dpp v94, v95, v94 row_ror:8 row_mask:0xf bank_mask:0xf
	v_cndmask_b32_e64 v95, v9, v94, s[46:47]
	v_cndmask_b32_e64 v9, v94, v9, s[46:47]
	s_nop 0
	v_mov_b32_dpp v94, v95 row_half_mirror row_mask:0xf bank_mask:0xf
	s_nop 1
	s_lshl_b64 s[26:27], s[26:27], 9
	s_ashr_i32 s29, s28, 31
	v_readlane_b32 s30, v96, 10
	s_add_u32 s66, s24, s62
	s_addc_u32 s67, s25, s63
	global_load_dwordx2 v[34:35], v121, s[66:67]
	s_waitcnt lgkmcnt(0)
	v_add_u32_dpp v9, v94, v9 quad_perm:[3,2,1,0] row_mask:0xf bank_mask:0xf
	s_nop 1
	s_lshl_b64 s[28:29], s[28:29], 9
	s_ashr_i32 s31, s30, 31
	v_readlane_b32 s34, v96, 11
	s_waitcnt lgkmcnt(0)
	v_add_u32_dpp v9, v9, v9 quad_perm:[2,3,0,1] row_mask:0xf bank_mask:0xf
	s_nop 1
	s_add_u32 s66, s26, s62
	s_addc_u32 s67, s27, s63
	global_load_dwordx2 v[36:37], v121, s[66:67]
	s_lshl_b64 s[30:31], s[30:31], 9
	s_ashr_i32 s35, s34, 31
	s_waitcnt lgkmcnt(0)
	v_add_u32_dpp v9, v9, v9 quad_perm:[1,0,3,2] row_mask:0xf bank_mask:0xf
	s_waitcnt vmcnt(10)
	v_mul_f32_e32 v7, v13, v7
	v_cvt_f32_i32_e32 v9, v9
	v_add_f32_e32 v9, v14, v9
	v_mul_f32_e32 v7, v7, v9
	v_mul_f32_e32 v9, 0x3d372713, v7
	v_mul_f32_e32 v9, v7, v9
	v_fma_f32 v9, v7, v9, v7
	v_mul_f32_e32 v9, 0x3fcc422a, v9
	v_mul_f32_e32 v9, 0xbfb8aa3b, v9
	v_exp_f32_e32 v9, v9
	v_readlane_b32 s38, v96, 12
	s_add_u32 s66, s28, s62
	s_addc_u32 s67, s29, s63
	global_load_dwordx2 v[38:39], v121, s[66:67]
	v_add_f32_e32 v9, 1.0, v9
	v_rcp_f32_e32 v9, v9
	s_lshl_b64 s[34:35], s[34:35], 9
	s_ashr_i32 s39, s38, 31
	s_lshl_b64 s[38:39], s[38:39], 9
	v_readlane_b32 s50, v96, 13
	v_readlane_b32 s52, v96, 14
	v_readlane_b32 s54, v96, 15
	s_ashr_i32 s51, s50, 31
	s_ashr_i32 s53, s52, 31
	s_ashr_i32 s55, s54, 31
	s_lshl_b64 s[50:51], s[50:51], 9
	s_lshl_b64 s[52:53], s[52:53], 9
	s_lshl_b64 s[54:55], s[54:55], 9
	s_add_u32 s66, s30, s62
	s_addc_u32 s67, s31, s63
	global_load_dwordx2 v[40:41], v121, s[66:67]
	s_add_u32 s66, s34, s62
	s_addc_u32 s67, s35, s63
	global_load_dwordx2 v[60:61], v121, s[66:67]
	s_add_u32 s66, s38, s62
	s_addc_u32 s67, s39, s63
	global_load_dwordx2 v[58:59], v121, s[66:67]
	s_add_u32 s66, s50, s62
	s_addc_u32 s67, s51, s63
	global_load_dwordx2 v[56:57], v121, s[66:67]
	s_add_u32 s66, s52, s62
	s_addc_u32 s67, s53, s63
	global_load_dwordx2 v[54:55], v121, s[66:67]
	s_add_u32 s66, s54, s62
	s_addc_u32 s67, s55, s63
	global_load_dwordx2 v[52:53], v121, s[66:67]
	v_pk_mul_f32 v[6:7], v[6:7], v[8:9]
	s_waitcnt vmcnt(34)
	v_alignbit_b32 v224, v92, v92, 4
	v_pk_mul_f32 v[6:7], v[6:7], v[6:7] op_sel:[0,1] op_sel_hi:[1,0]
	v_cvt_f16_f32_e32 v120, v6
	v_and_b32_e32 v8, 0x7070707, v92
	v_readlane_b32 s36, v120, 0
	v_and_b32_e32 v9, 0x7070707, v224
	v_perm_b32 v8, s2, v205, v8
	v_perm_b32 v9, s2, v205, v9
	v_and_or_b32 v8, v92, s4, v8
	v_and_or_b32 v9, v224, s4, v9
	v_perm_b32 v92, v9, v8, s5
	v_perm_b32 v94, v9, v8, s33
	v_perm_b32 v95, v9, v8, s0
	v_perm_b32 v8, v9, v8, s1
	v_pk_fma_f16 v8, v8, s36, v102 op_sel_hi:[1,0,1]
	v_alignbit_b32 v225, v93, v93, 4
	v_pk_fma_f16 v9, v92, s36, v105 op_sel_hi:[1,0,1]
	v_pk_fma_f16 v92, v94, s36, v104 op_sel_hi:[1,0,1]
	v_pk_fma_f16 v94, v95, s36, v103 op_sel_hi:[1,0,1]
	v_and_b32_e32 v95, 0x7070707, v93
	v_and_b32_e32 v102, 0x7070707, v225
	v_perm_b32 v95, s2, v205, v95
	v_perm_b32 v102, s2, v205, v102
	v_and_or_b32 v95, v93, s4, v95
	v_and_or_b32 v93, v225, s4, v102
	v_perm_b32 v102, v93, v95, s5
	v_perm_b32 v103, v93, v95, s33
	v_perm_b32 v104, v93, v95, s0
	v_perm_b32 v93, v93, v95, s1
	v_pk_fma_f16 v95, v102, s36, v101 op_sel_hi:[1,0,1]
	v_readlane_b32 s59, v120, 4
	s_waitcnt vmcnt(33)
	v_alignbit_b32 v224, v90, v90, 4
	v_pk_fma_f16 v100, v103, s36, v100 op_sel_hi:[1,0,1]
	v_pk_fma_f16 v99, v104, s36, v99 op_sel_hi:[1,0,1]
	v_pk_fma_f16 v7, v93, s36, v15 op_sel_hi:[1,0,1]
	s_setprio 0
	v_and_b32_e32 v93, 0x7070707, v90
	v_and_b32_e32 v101, 0x7070707, v224
	v_perm_b32 v93, s2, v205, v93
	v_perm_b32 v101, s2, v205, v101
	v_and_or_b32 v93, v90, s4, v93
	v_and_or_b32 v90, v224, s4, v101
	v_perm_b32 v103, v90, v93, s0
	v_perm_b32 v101, v90, v93, s5
	v_perm_b32 v102, v90, v93, s33
	v_perm_b32 v90, v90, v93, s1
	v_pk_fma_f16 v93, v103, s59, v94 op_sel_hi:[1,0,1]
	v_alignbit_b32 v225, v91, v91, 4
	v_pk_fma_f16 v8, v90, s59, v8 op_sel_hi:[1,0,1]
	v_and_b32_e32 v90, 0x7070707, v91
	v_and_b32_e32 v94, 0x7070707, v225
	v_pk_fma_f16 v9, v101, s59, v9 op_sel_hi:[1,0,1]
	v_perm_b32 v90, s2, v205, v90
	v_perm_b32 v94, s2, v205, v94
	v_and_or_b32 v90, v91, s4, v90
	v_and_or_b32 v91, v225, s4, v94
	v_pk_fma_f16 v92, v102, s59, v92 op_sel_hi:[1,0,1]
	v_perm_b32 v94, v91, v90, s5
	v_perm_b32 v102, v91, v90, s0
	v_perm_b32 v101, v91, v90, s33
	v_perm_b32 v90, v91, v90, s1
	v_pk_fma_f16 v91, v94, s59, v95 op_sel_hi:[1,0,1]
	v_pk_fma_f16 v95, v102, s59, v99 op_sel_hi:[1,0,1]
	v_readlane_b32 s60, v120, 8
	s_waitcnt vmcnt(32)
	v_alignbit_b32 v224, v88, v88, 4
	v_pk_fma_f16 v94, v101, s59, v100 op_sel_hi:[1,0,1]
	v_pk_fma_f16 v7, v90, s59, v7 op_sel_hi:[1,0,1]
	v_and_b32_e32 v90, 0x7070707, v88
	v_and_b32_e32 v99, 0x7070707, v224
	v_perm_b32 v90, s2, v205, v90
	v_perm_b32 v99, s2, v205, v99
	v_and_or_b32 v90, v88, s4, v90
	v_and_or_b32 v88, v224, s4, v99
	v_perm_b32 v100, v88, v90, s33
	v_perm_b32 v101, v88, v90, s0
	v_perm_b32 v99, v88, v90, s5
	v_perm_b32 v88, v88, v90, s1
	v_pk_fma_f16 v90, v100, s60, v92 op_sel_hi:[1,0,1]
	v_pk_fma_f16 v92, v101, s60, v93 op_sel_hi:[1,0,1]
	v_alignbit_b32 v225, v89, v89, 4
	v_pk_fma_f16 v8, v88, s60, v8 op_sel_hi:[1,0,1]
	v_and_b32_e32 v88, 0x7070707, v89
	v_and_b32_e32 v93, 0x7070707, v225
	v_pk_fma_f16 v9, v99, s60, v9 op_sel_hi:[1,0,1]
	v_perm_b32 v88, s2, v205, v88
	v_perm_b32 v93, s2, v205, v93
	v_and_or_b32 v88, v89, s4, v88
	v_and_or_b32 v89, v225, s4, v93
	v_perm_b32 v93, v89, v88, s5
	v_perm_b32 v99, v89, v88, s33
	v_perm_b32 v100, v89, v88, s0
	v_perm_b32 v88, v89, v88, s1
	v_pk_fma_f16 v89, v93, s60, v91 op_sel_hi:[1,0,1]
	v_pk_fma_f16 v91, v99, s60, v94 op_sel_hi:[1,0,1]
	v_readlane_b32 s36, v120, 12
	s_waitcnt vmcnt(31)
	v_alignbit_b32 v224, v86, v86, 4
	v_pk_fma_f16 v93, v100, s60, v95 op_sel_hi:[1,0,1]
	v_pk_fma_f16 v7, v88, s60, v7 op_sel_hi:[1,0,1]
	v_and_b32_e32 v88, 0x7070707, v86
	v_and_b32_e32 v94, 0x7070707, v224
	v_perm_b32 v88, s2, v205, v88
	v_perm_b32 v94, s2, v205, v94
	v_and_or_b32 v88, v86, s4, v88
	v_and_or_b32 v86, v224, s4, v94
	v_perm_b32 v95, v86, v88, s33
	v_perm_b32 v99, v86, v88, s0
	v_perm_b32 v94, v86, v88, s5
	v_perm_b32 v86, v86, v88, s1
	v_pk_fma_f16 v88, v95, s36, v90 op_sel_hi:[1,0,1]
	v_pk_fma_f16 v90, v99, s36, v92 op_sel_hi:[1,0,1]
	v_alignbit_b32 v225, v87, v87, 4
	v_pk_fma_f16 v8, v86, s36, v8 op_sel_hi:[1,0,1]
	v_and_b32_e32 v86, 0x7070707, v87
	v_and_b32_e32 v92, 0x7070707, v225
	v_pk_fma_f16 v9, v94, s36, v9 op_sel_hi:[1,0,1]
	v_perm_b32 v86, s2, v205, v86
	v_perm_b32 v92, s2, v205, v92
	v_and_or_b32 v86, v87, s4, v86
	v_and_or_b32 v87, v225, s4, v92
	v_perm_b32 v92, v87, v86, s5
	v_perm_b32 v94, v87, v86, s33
	v_perm_b32 v95, v87, v86, s0
	v_perm_b32 v86, v87, v86, s1
	v_pk_fma_f16 v87, v92, s36, v89 op_sel_hi:[1,0,1]
	v_readlane_b32 s59, v120, 16
	s_waitcnt vmcnt(30)
	v_alignbit_b32 v224, v84, v84, 4
	v_pk_fma_f16 v89, v94, s36, v91 op_sel_hi:[1,0,1]
	v_pk_fma_f16 v91, v95, s36, v93 op_sel_hi:[1,0,1]
	v_pk_fma_f16 v7, v86, s36, v7 op_sel_hi:[1,0,1]
	v_and_b32_e32 v86, 0x7070707, v84
	v_and_b32_e32 v92, 0x7070707, v224
	v_perm_b32 v86, s2, v205, v86
	v_perm_b32 v92, s2, v205, v92
	v_and_or_b32 v86, v84, s4, v86
	v_and_or_b32 v84, v224, s4, v92
	v_perm_b32 v93, v84, v86, s33
	v_perm_b32 v94, v84, v86, s0
	v_perm_b32 v92, v84, v86, s5
	v_perm_b32 v84, v84, v86, s1
	v_pk_fma_f16 v86, v93, s59, v88 op_sel_hi:[1,0,1]
	v_pk_fma_f16 v88, v94, s59, v90 op_sel_hi:[1,0,1]
	v_alignbit_b32 v225, v85, v85, 4
	v_pk_fma_f16 v8, v84, s59, v8 op_sel_hi:[1,0,1]
	v_and_b32_e32 v84, 0x7070707, v85
	v_and_b32_e32 v90, 0x7070707, v225
	v_pk_fma_f16 v9, v92, s59, v9 op_sel_hi:[1,0,1]
	v_perm_b32 v84, s2, v205, v84
	v_perm_b32 v90, s2, v205, v90
	v_and_or_b32 v84, v85, s4, v84
	v_and_or_b32 v85, v225, s4, v90
	v_perm_b32 v90, v85, v84, s5
	v_perm_b32 v92, v85, v84, s33
	v_perm_b32 v93, v85, v84, s0
	v_perm_b32 v84, v85, v84, s1
	v_pk_fma_f16 v85, v90, s59, v87 op_sel_hi:[1,0,1]
	v_readlane_b32 s60, v120, 20
	s_waitcnt vmcnt(29)
	v_alignbit_b32 v224, v82, v82, 4
	v_pk_fma_f16 v87, v92, s59, v89 op_sel_hi:[1,0,1]
	v_pk_fma_f16 v89, v93, s59, v91 op_sel_hi:[1,0,1]
	v_pk_fma_f16 v7, v84, s59, v7 op_sel_hi:[1,0,1]
	v_and_b32_e32 v84, 0x7070707, v82
	v_and_b32_e32 v90, 0x7070707, v224
	v_perm_b32 v84, s2, v205, v84
	v_perm_b32 v90, s2, v205, v90
	v_and_or_b32 v84, v82, s4, v84
	v_and_or_b32 v82, v224, s4, v90
	v_perm_b32 v91, v82, v84, s33
	v_perm_b32 v92, v82, v84, s0
	v_perm_b32 v90, v82, v84, s5
	v_perm_b32 v82, v82, v84, s1
	v_pk_fma_f16 v84, v91, s60, v86 op_sel_hi:[1,0,1]
	v_pk_fma_f16 v86, v92, s60, v88 op_sel_hi:[1,0,1]
	s_add_u32 s66, s10, s64
	s_addc_u32 s67, s11, s65
	global_load_dwordx2 v[92:93], v121, s[66:67]
	v_alignbit_b32 v225, v83, v83, 4
	v_pk_fma_f16 v8, v82, s60, v8 op_sel_hi:[1,0,1]
	v_and_b32_e32 v82, 0x7070707, v83
	v_and_b32_e32 v88, 0x7070707, v225
	v_pk_fma_f16 v9, v90, s60, v9 op_sel_hi:[1,0,1]
	v_perm_b32 v82, s2, v205, v82
	v_perm_b32 v88, s2, v205, v88
	v_and_or_b32 v82, v83, s4, v82
	v_and_or_b32 v83, v225, s4, v88
	v_perm_b32 v88, v83, v82, s5
	v_perm_b32 v90, v83, v82, s33
	v_perm_b32 v91, v83, v82, s0
	v_perm_b32 v82, v83, v82, s1
	v_pk_fma_f16 v83, v88, s60, v85 op_sel_hi:[1,0,1]
	v_readlane_b32 s36, v120, 24
	s_waitcnt vmcnt(29)
	v_alignbit_b32 v224, v80, v80, 4
	v_pk_fma_f16 v85, v90, s60, v87 op_sel_hi:[1,0,1]
	v_pk_fma_f16 v87, v91, s60, v89 op_sel_hi:[1,0,1]
	v_pk_fma_f16 v7, v82, s60, v7 op_sel_hi:[1,0,1]
	v_and_b32_e32 v82, 0x7070707, v80
	v_and_b32_e32 v88, 0x7070707, v224
	v_perm_b32 v82, s2, v205, v82
	v_perm_b32 v88, s2, v205, v88
	v_and_or_b32 v82, v80, s4, v82
	v_and_or_b32 v80, v224, s4, v88
	v_perm_b32 v89, v80, v82, s33
	v_perm_b32 v90, v80, v82, s0
	v_perm_b32 v88, v80, v82, s5
	v_perm_b32 v80, v80, v82, s1
	v_pk_fma_f16 v82, v89, s36, v84 op_sel_hi:[1,0,1]
	v_pk_fma_f16 v84, v90, s36, v86 op_sel_hi:[1,0,1]
	s_add_u32 s66, s12, s64
	s_addc_u32 s67, s13, s65
	global_load_dwordx2 v[90:91], v121, s[66:67]
	v_alignbit_b32 v225, v81, v81, 4
	v_pk_fma_f16 v8, v80, s36, v8 op_sel_hi:[1,0,1]
	v_and_b32_e32 v80, 0x7070707, v81
	v_and_b32_e32 v86, 0x7070707, v225
	v_pk_fma_f16 v9, v88, s36, v9 op_sel_hi:[1,0,1]
	v_perm_b32 v80, s2, v205, v80
	v_perm_b32 v86, s2, v205, v86
	v_and_or_b32 v80, v81, s4, v80
	v_and_or_b32 v81, v225, s4, v86
	v_perm_b32 v86, v81, v80, s5
	v_perm_b32 v88, v81, v80, s33
	v_perm_b32 v89, v81, v80, s0
	v_perm_b32 v80, v81, v80, s1
	v_pk_fma_f16 v81, v86, s36, v83 op_sel_hi:[1,0,1]
	v_readlane_b32 s59, v120, 28
	s_waitcnt vmcnt(29)
	v_alignbit_b32 v224, v78, v78, 4
	v_pk_fma_f16 v83, v88, s36, v85 op_sel_hi:[1,0,1]
	v_pk_fma_f16 v85, v89, s36, v87 op_sel_hi:[1,0,1]
	v_pk_fma_f16 v7, v80, s36, v7 op_sel_hi:[1,0,1]
	v_and_b32_e32 v80, 0x7070707, v78
	v_and_b32_e32 v86, 0x7070707, v224
	v_perm_b32 v80, s2, v205, v80
	v_perm_b32 v86, s2, v205, v86
	v_and_or_b32 v80, v78, s4, v80
	v_and_or_b32 v78, v224, s4, v86
	v_perm_b32 v87, v78, v80, s33
	v_perm_b32 v88, v78, v80, s0
	v_perm_b32 v86, v78, v80, s5
	v_perm_b32 v78, v78, v80, s1
	v_pk_fma_f16 v80, v87, s59, v82 op_sel_hi:[1,0,1]
	v_pk_fma_f16 v82, v88, s59, v84 op_sel_hi:[1,0,1]
	s_add_u32 s66, s14, s64
	s_addc_u32 s67, s15, s65
	global_load_dwordx2 v[88:89], v121, s[66:67]
	v_alignbit_b32 v225, v79, v79, 4
	v_pk_fma_f16 v8, v78, s59, v8 op_sel_hi:[1,0,1]
	v_and_b32_e32 v78, 0x7070707, v79
	v_and_b32_e32 v84, 0x7070707, v225
	v_pk_fma_f16 v9, v86, s59, v9 op_sel_hi:[1,0,1]
	v_perm_b32 v78, s2, v205, v78
	v_perm_b32 v84, s2, v205, v84
	v_and_or_b32 v78, v79, s4, v78
	v_and_or_b32 v79, v225, s4, v84
	v_perm_b32 v84, v79, v78, s5
	v_perm_b32 v86, v79, v78, s33
	v_perm_b32 v87, v79, v78, s0
	v_perm_b32 v78, v79, v78, s1
	v_pk_fma_f16 v79, v84, s59, v81 op_sel_hi:[1,0,1]
	v_readlane_b32 s60, v120, 32
	s_waitcnt vmcnt(29)
	v_alignbit_b32 v224, v76, v76, 4
	v_pk_fma_f16 v81, v86, s59, v83 op_sel_hi:[1,0,1]
	v_pk_fma_f16 v83, v87, s59, v85 op_sel_hi:[1,0,1]
	v_pk_fma_f16 v7, v78, s59, v7 op_sel_hi:[1,0,1]
	v_and_b32_e32 v78, 0x7070707, v76
	v_and_b32_e32 v84, 0x7070707, v224
	v_perm_b32 v78, s2, v205, v78
	v_perm_b32 v84, s2, v205, v84
	v_and_or_b32 v78, v76, s4, v78
	v_and_or_b32 v76, v224, s4, v84
	v_perm_b32 v85, v76, v78, s33
	v_perm_b32 v86, v76, v78, s0
	v_perm_b32 v84, v76, v78, s5
	v_perm_b32 v76, v76, v78, s1
	v_pk_fma_f16 v78, v85, s60, v80 op_sel_hi:[1,0,1]
	v_pk_fma_f16 v80, v86, s60, v82 op_sel_hi:[1,0,1]
	s_add_u32 s66, s16, s64
	s_addc_u32 s67, s17, s65
	global_load_dwordx2 v[86:87], v121, s[66:67]
	v_alignbit_b32 v225, v77, v77, 4
	v_pk_fma_f16 v8, v76, s60, v8 op_sel_hi:[1,0,1]
	v_and_b32_e32 v76, 0x7070707, v77
	v_and_b32_e32 v82, 0x7070707, v225
	v_pk_fma_f16 v9, v84, s60, v9 op_sel_hi:[1,0,1]
	v_perm_b32 v76, s2, v205, v76
	v_perm_b32 v82, s2, v205, v82
	v_and_or_b32 v76, v77, s4, v76
	v_and_or_b32 v77, v225, s4, v82
	v_perm_b32 v82, v77, v76, s5
	v_perm_b32 v84, v77, v76, s33
	v_perm_b32 v85, v77, v76, s0
	v_perm_b32 v76, v77, v76, s1
	v_pk_fma_f16 v77, v82, s60, v79 op_sel_hi:[1,0,1]
	v_readlane_b32 s36, v120, 36
	s_waitcnt vmcnt(28)
	v_alignbit_b32 v224, v70, v70, 4
	v_pk_fma_f16 v79, v84, s60, v81 op_sel_hi:[1,0,1]
	v_pk_fma_f16 v81, v85, s60, v83 op_sel_hi:[1,0,1]
	v_pk_fma_f16 v7, v76, s60, v7 op_sel_hi:[1,0,1]
	v_and_b32_e32 v76, 0x7070707, v70
	v_and_b32_e32 v82, 0x7070707, v224
	v_perm_b32 v76, s2, v205, v76
	v_perm_b32 v82, s2, v205, v82
	v_and_or_b32 v76, v70, s4, v76
	v_and_or_b32 v70, v224, s4, v82
	v_perm_b32 v83, v70, v76, s33
	v_perm_b32 v84, v70, v76, s0
	v_perm_b32 v82, v70, v76, s5
	v_perm_b32 v70, v70, v76, s1
	v_pk_fma_f16 v76, v83, s36, v78 op_sel_hi:[1,0,1]
	v_pk_fma_f16 v78, v84, s36, v80 op_sel_hi:[1,0,1]
	s_add_u32 s66, s18, s64
	s_addc_u32 s67, s19, s65
	global_load_dwordx2 v[84:85], v121, s[66:67]
	v_alignbit_b32 v225, v71, v71, 4
	v_pk_fma_f16 v8, v70, s36, v8 op_sel_hi:[1,0,1]
	v_and_b32_e32 v70, 0x7070707, v71
	v_and_b32_e32 v80, 0x7070707, v225
	v_pk_fma_f16 v9, v82, s36, v9 op_sel_hi:[1,0,1]
	v_perm_b32 v70, s2, v205, v70
	v_perm_b32 v80, s2, v205, v80
	v_and_or_b32 v70, v71, s4, v70
	v_and_or_b32 v71, v225, s4, v80
	v_perm_b32 v80, v71, v70, s5
	v_perm_b32 v82, v71, v70, s33
	v_perm_b32 v83, v71, v70, s0
	v_perm_b32 v70, v71, v70, s1
	v_pk_fma_f16 v71, v80, s36, v77 op_sel_hi:[1,0,1]
	v_readlane_b32 s59, v120, 40
	s_waitcnt vmcnt(25)
	v_alignbit_b32 v224, v66, v66, 4
	v_pk_fma_f16 v77, v82, s36, v79 op_sel_hi:[1,0,1]
	v_pk_fma_f16 v79, v83, s36, v81 op_sel_hi:[1,0,1]
	v_pk_fma_f16 v7, v70, s36, v7 op_sel_hi:[1,0,1]
	v_and_b32_e32 v70, 0x7070707, v66
	v_and_b32_e32 v80, 0x7070707, v224
	v_perm_b32 v70, s2, v205, v70
	v_perm_b32 v80, s2, v205, v80
	v_and_or_b32 v70, v66, s4, v70
	v_and_or_b32 v66, v224, s4, v80
	v_perm_b32 v81, v66, v70, s33
	v_perm_b32 v82, v66, v70, s0
	v_perm_b32 v80, v66, v70, s5
	v_perm_b32 v66, v66, v70, s1
	v_pk_fma_f16 v70, v81, s59, v76 op_sel_hi:[1,0,1]
	v_pk_fma_f16 v76, v82, s59, v78 op_sel_hi:[1,0,1]
	s_add_u32 s66, s20, s64
	s_addc_u32 s67, s21, s65
	global_load_dwordx2 v[82:83], v121, s[66:67]
	v_alignbit_b32 v225, v67, v67, 4
	v_pk_fma_f16 v8, v66, s59, v8 op_sel_hi:[1,0,1]
	v_and_b32_e32 v66, 0x7070707, v67
	v_and_b32_e32 v78, 0x7070707, v225
	v_pk_fma_f16 v9, v80, s59, v9 op_sel_hi:[1,0,1]
	v_perm_b32 v66, s2, v205, v66
	v_perm_b32 v78, s2, v205, v78
	v_and_or_b32 v66, v67, s4, v66
	v_and_or_b32 v67, v225, s4, v78
	v_perm_b32 v78, v67, v66, s5
	v_perm_b32 v80, v67, v66, s33
	v_perm_b32 v81, v67, v66, s0
	v_perm_b32 v66, v67, v66, s1
	v_pk_fma_f16 v67, v78, s59, v71 op_sel_hi:[1,0,1]
	v_readlane_b32 s60, v120, 44
	s_waitcnt vmcnt(31)
	v_alignbit_b32 v224, v72, v72, 4
	v_pk_fma_f16 v71, v80, s59, v77 op_sel_hi:[1,0,1]
	v_pk_fma_f16 v77, v81, s59, v79 op_sel_hi:[1,0,1]
	v_pk_fma_f16 v7, v66, s59, v7 op_sel_hi:[1,0,1]
	v_and_b32_e32 v66, 0x7070707, v72
	v_and_b32_e32 v78, 0x7070707, v224
	v_perm_b32 v66, s2, v205, v66
	v_perm_b32 v78, s2, v205, v78
	v_and_or_b32 v66, v72, s4, v66
	v_and_or_b32 v72, v224, s4, v78
	v_perm_b32 v80, v72, v66, s0
	v_perm_b32 v78, v72, v66, s5
	v_perm_b32 v79, v72, v66, s33
	v_perm_b32 v66, v72, v66, s1
	v_pk_fma_f16 v72, v80, s60, v76 op_sel_hi:[1,0,1]
	s_add_u32 s66, s22, s64
	s_addc_u32 s67, s23, s65
	global_load_dwordx2 v[80:81], v121, s[66:67]
	v_alignbit_b32 v225, v73, v73, 4
	v_pk_fma_f16 v8, v66, s60, v8 op_sel_hi:[1,0,1]
	v_and_b32_e32 v66, 0x7070707, v73
	v_and_b32_e32 v76, 0x7070707, v225
	v_pk_fma_f16 v9, v78, s60, v9 op_sel_hi:[1,0,1]
	v_perm_b32 v66, s2, v205, v66
	v_perm_b32 v76, s2, v205, v76
	v_and_or_b32 v66, v73, s4, v66
	v_and_or_b32 v73, v225, s4, v76
	v_perm_b32 v76, v73, v66, s5
	v_pk_fma_f16 v70, v79, s60, v70 op_sel_hi:[1,0,1]
	v_perm_b32 v78, v73, v66, s33
	v_perm_b32 v79, v73, v66, s0
	v_perm_b32 v66, v73, v66, s1
	v_pk_fma_f16 v67, v76, s60, v67 op_sel_hi:[1,0,1]
	v_readlane_b32 s36, v120, 48
	s_waitcnt vmcnt(30)
	v_alignbit_b32 v224, v68, v68, 4
	v_pk_fma_f16 v71, v78, s60, v71 op_sel_hi:[1,0,1]
	v_pk_fma_f16 v73, v79, s60, v77 op_sel_hi:[1,0,1]
	v_pk_fma_f16 v7, v66, s60, v7 op_sel_hi:[1,0,1]
	v_and_b32_e32 v66, 0x7070707, v68
	v_and_b32_e32 v76, 0x7070707, v224
	v_perm_b32 v66, s2, v205, v66
	v_perm_b32 v76, s2, v205, v76
	v_and_or_b32 v66, v68, s4, v66
	v_and_or_b32 v68, v224, s4, v76
	v_perm_b32 v77, v68, v66, s33
	v_perm_b32 v78, v68, v66, s0
	v_perm_b32 v76, v68, v66, s5
	v_perm_b32 v66, v68, v66, s1
	v_pk_fma_f16 v68, v77, s36, v70 op_sel_hi:[1,0,1]
	v_pk_fma_f16 v70, v78, s36, v72 op_sel_hi:[1,0,1]
	s_add_u32 s66, s24, s64
	s_addc_u32 s67, s25, s65
	global_load_dwordx2 v[78:79], v121, s[66:67]
	v_alignbit_b32 v225, v69, v69, 4
	v_pk_fma_f16 v8, v66, s36, v8 op_sel_hi:[1,0,1]
	v_and_b32_e32 v66, 0x7070707, v69
	v_and_b32_e32 v72, 0x7070707, v225
	v_pk_fma_f16 v9, v76, s36, v9 op_sel_hi:[1,0,1]
	v_perm_b32 v66, s2, v205, v66
	v_perm_b32 v72, s2, v205, v72
	v_and_or_b32 v66, v69, s4, v66
	v_and_or_b32 v69, v225, s4, v72
	v_perm_b32 v72, v69, v66, s5
	v_perm_b32 v76, v69, v66, s33
	v_perm_b32 v77, v69, v66, s0
	v_perm_b32 v66, v69, v66, s1
	v_pk_fma_f16 v67, v72, s36, v67 op_sel_hi:[1,0,1]
	v_readlane_b32 s59, v120, 52
	s_waitcnt vmcnt(29)
	v_alignbit_b32 v224, v64, v64, 4
	v_pk_fma_f16 v69, v76, s36, v71 op_sel_hi:[1,0,1]
	v_pk_fma_f16 v71, v77, s36, v73 op_sel_hi:[1,0,1]
	v_pk_fma_f16 v7, v66, s36, v7 op_sel_hi:[1,0,1]
	v_and_b32_e32 v66, 0x7070707, v64
	v_and_b32_e32 v72, 0x7070707, v224
	v_perm_b32 v66, s2, v205, v66
	v_perm_b32 v72, s2, v205, v72
	v_and_or_b32 v66, v64, s4, v66
	v_and_or_b32 v64, v224, s4, v72
	v_perm_b32 v73, v64, v66, s33
	v_perm_b32 v76, v64, v66, s0
	v_perm_b32 v72, v64, v66, s5
	v_perm_b32 v64, v64, v66, s1
	v_pk_fma_f16 v66, v73, s59, v68 op_sel_hi:[1,0,1]
	v_pk_fma_f16 v68, v76, s59, v70 op_sel_hi:[1,0,1]
	s_add_u32 s66, s26, s64
	s_addc_u32 s67, s27, s65
	global_load_dwordx2 v[76:77], v121, s[66:67]
	v_alignbit_b32 v225, v65, v65, 4
	v_pk_fma_f16 v8, v64, s59, v8 op_sel_hi:[1,0,1]
	v_and_b32_e32 v64, 0x7070707, v65
	v_and_b32_e32 v70, 0x7070707, v225
	v_pk_fma_f16 v9, v72, s59, v9 op_sel_hi:[1,0,1]
	v_perm_b32 v64, s2, v205, v64
	v_perm_b32 v70, s2, v205, v70
	v_and_or_b32 v64, v65, s4, v64
	v_and_or_b32 v65, v225, s4, v70
	v_perm_b32 v70, v65, v64, s5
	v_perm_b32 v72, v65, v64, s33
	v_perm_b32 v73, v65, v64, s0
	v_perm_b32 v64, v65, v64, s1
	v_pk_fma_f16 v65, v70, s59, v67 op_sel_hi:[1,0,1]
	v_readlane_b32 s60, v120, 56
	s_waitcnt vmcnt(31)
	v_alignbit_b32 v224, v62, v62, 4
	v_pk_fma_f16 v67, v72, s59, v69 op_sel_hi:[1,0,1]
	v_pk_fma_f16 v69, v73, s59, v71 op_sel_hi:[1,0,1]
	v_pk_fma_f16 v7, v64, s59, v7 op_sel_hi:[1,0,1]
	v_and_b32_e32 v64, 0x7070707, v62
	v_and_b32_e32 v70, 0x7070707, v224
	v_perm_b32 v64, s2, v205, v64
	v_perm_b32 v70, s2, v205, v70
	v_and_or_b32 v64, v62, s4, v64
	v_and_or_b32 v62, v224, s4, v70
	v_perm_b32 v71, v62, v64, s33
	v_perm_b32 v72, v62, v64, s0
	v_perm_b32 v70, v62, v64, s5
	v_perm_b32 v62, v62, v64, s1
	v_pk_fma_f16 v64, v71, s60, v66 op_sel_hi:[1,0,1]
	v_pk_fma_f16 v66, v72, s60, v68 op_sel_hi:[1,0,1]
	s_add_u32 s66, s34, s64
	s_addc_u32 s67, s35, s65
	global_load_dwordx2 v[72:73], v121, s[66:67]
	v_alignbit_b32 v225, v63, v63, 4
	v_pk_fma_f16 v8, v62, s60, v8 op_sel_hi:[1,0,1]
	v_and_b32_e32 v62, 0x7070707, v63
	v_and_b32_e32 v68, 0x7070707, v225
	v_pk_fma_f16 v9, v70, s60, v9 op_sel_hi:[1,0,1]
	v_perm_b32 v62, s2, v205, v62
	v_perm_b32 v68, s2, v205, v68
	v_and_or_b32 v62, v63, s4, v62
	v_and_or_b32 v63, v225, s4, v68
	v_perm_b32 v68, v63, v62, s5
	v_perm_b32 v70, v63, v62, s33
	v_perm_b32 v71, v63, v62, s0
	v_perm_b32 v62, v63, v62, s1
	v_pk_fma_f16 v7, v62, s60, v7 op_sel_hi:[1,0,1]
	v_readlane_b32 s36, v120, 60
	s_waitcnt vmcnt(29)
	v_alignbit_b32 v224, v50, v50, 4
	v_pk_fma_f16 v63, v68, s60, v65 op_sel_hi:[1,0,1]
	v_pk_fma_f16 v65, v70, s60, v67 op_sel_hi:[1,0,1]
	v_pk_fma_f16 v67, v71, s60, v69 op_sel_hi:[1,0,1]
	s_add_u32 s66, s28, s64
	s_addc_u32 s67, s29, s65
	global_load_dwordx2 v[70:71], v121, s[66:67]
	v_and_b32_e32 v15, 0x7070707, v50
	v_and_b32_e32 v62, 0x7070707, v224
	v_perm_b32 v15, s2, v205, v15
	v_perm_b32 v62, s2, v205, v62
	v_and_or_b32 v15, v50, s4, v15
	v_and_or_b32 v50, v224, s4, v62
	v_perm_b32 v62, v50, v15, s5
	v_perm_b32 v68, v50, v15, s33
	v_perm_b32 v69, v50, v15, s0
	v_perm_b32 v15, v50, v15, s1
	v_pk_fma_f16 v105, v62, s36, v9 op_sel_hi:[1,0,1]
	v_alignbit_b32 v225, v51, v51, 4
	v_pk_fma_f16 v102, v15, s36, v8 op_sel_hi:[1,0,1]
	v_and_b32_e32 v8, 0x7070707, v51
	v_and_b32_e32 v9, 0x7070707, v225
	v_perm_b32 v8, s2, v205, v8
	v_perm_b32 v9, s2, v205, v9
	v_and_or_b32 v8, v51, s4, v8
	v_and_or_b32 v9, v225, s4, v9
	v_perm_b32 v15, v9, v8, s5
	v_perm_b32 v50, v9, v8, s33
	v_perm_b32 v51, v9, v8, s0
	v_perm_b32 v8, v9, v8, s1
	v_pk_fma_f16 v104, v68, s36, v64 op_sel_hi:[1,0,1]
	v_pk_fma_f16 v103, v69, s36, v66 op_sel_hi:[1,0,1]
	s_add_u32 s66, s38, s64
	s_addc_u32 s67, s39, s65
	global_load_dwordx2 v[68:69], v121, s[66:67]
	v_pk_fma_f16 v101, v15, s36, v63 op_sel_hi:[1,0,1]
	s_add_u32 s66, s52, s64
	s_addc_u32 s67, s53, s65
	global_load_dwordx2 v[62:63], v121, s[66:67]
	v_pk_fma_f16 v100, v50, s36, v65 op_sel_hi:[1,0,1]
	s_add_u32 s66, s50, s64
	s_addc_u32 s67, s51, s65
	global_load_dwordx2 v[64:65], v121, s[66:67]
	v_pk_fma_f16 v99, v51, s36, v67 op_sel_hi:[1,0,1]
	s_add_u32 s66, s30, s64
	s_addc_u32 s67, s31, s65
	global_load_dwordx2 v[66:67], v121, s[66:67]
	s_add_u32 s66, s54, s64
	s_addc_u32 s67, s55, s65
	global_load_dwordx2 v[50:51], v121, s[66:67]
	v_pk_fma_f16 v15, v8, s36, v7 op_sel_hi:[1,0,1]
	s_cmpk_eq_i32 s56, 0x90
	s_cbranch_scc0 .LBB0_770
	v_lshl_add_u64 v[94:95], v[2:3], 2, v[44:45]
	v_mov_b32_e32 v106, v208
	v_mov_b32_e32 v107, v209
	v_mov_b32_e32 v108, v210
	v_mov_b32_e32 v109, v211
	v_mov_b32_e32 v8, v212
	v_mov_b32_e32 v9, v213
	v_mov_b32_e32 v10, v214
	v_mov_b32_e32 v11, v215
	v_mov_b32_e32 v4, v216
	v_mov_b32_e32 v5, v217
	v_mov_b32_e32 v6, v218
	v_mov_b32_e32 v7, v219
	v_mov_b32_e32 v0, v220
	v_mov_b32_e32 v1, v221
	v_mov_b32_e32 v2, v222
	v_mov_b32_e32 v3, v223
	v_cvt_f32_f16_sdwa v13, v105 dst_sel:DWORD dst_unused:UNUSED_PAD src0_sel:WORD_1
	v_cvt_f32_f16_e32 v12, v105
	s_mov_b32 s12, 0x800000
	v_readlane_b32 s10, v255, 5
	v_readlane_b32 s11, v255, 6
	v_pk_add_f32 v[0:1], v[0:1], v[12:13]
	v_cvt_f32_f16_sdwa v13, v104 dst_sel:DWORD dst_unused:UNUSED_PAD src0_sel:WORD_1
	v_cvt_f32_f16_e32 v12, v104
	v_lshl_add_u64 v[48:49], v[48:49], 0, s[10:11]
	v_pk_add_f32 v[2:3], v[2:3], v[12:13]
	v_cvt_f32_f16_sdwa v13, v103 dst_sel:DWORD dst_unused:UNUSED_PAD src0_sel:WORD_1
	v_cvt_f32_f16_e32 v12, v103
	global_store_dwordx4 v[94:95], v[0:3], off
	v_pk_add_f32 v[4:5], v[4:5], v[12:13]
	v_cvt_f32_f16_sdwa v13, v102 dst_sel:DWORD dst_unused:UNUSED_PAD src0_sel:WORD_1
	v_cvt_f32_f16_e32 v12, v102
	v_mov_b32_e32 v102, v1
	v_mov_b32_e32 v103, v5
	v_pk_mul_f32 v[102:103], v[102:103], v[102:103]
	v_pk_add_f32 v[6:7], v[6:7], v[12:13]
	v_mov_b32_e32 v12, v0
	v_mov_b32_e32 v13, v4
	v_pk_fma_f32 v[12:13], v[12:13], v[12:13], v[102:103]
	v_mov_b32_e32 v102, v2
	v_mov_b32_e32 v103, v6
	v_pk_fma_f32 v[12:13], v[102:103], v[102:103], v[12:13]
	v_mov_b32_e32 v102, v3
	v_mov_b32_e32 v103, v7
	v_pk_fma_f32 v[102:103], v[102:103], v[102:103], v[12:13]
	v_cvt_f32_f16_sdwa v13, v101 dst_sel:DWORD dst_unused:UNUSED_PAD src0_sel:WORD_1
	v_cvt_f32_f16_e32 v12, v101
	v_cvt_f32_f16_sdwa v101, v15 dst_sel:DWORD dst_unused:UNUSED_PAD src0_sel:WORD_1
	global_store_dwordx4 v[94:95], v[4:7], off offset:16
	v_pk_add_f32 v[8:9], v[8:9], v[12:13]
	v_cvt_f32_f16_sdwa v13, v100 dst_sel:DWORD dst_unused:UNUSED_PAD src0_sel:WORD_1
	v_cvt_f32_f16_e32 v12, v100
	v_cvt_f32_f16_e32 v100, v15
	v_pk_add_f32 v[10:11], v[10:11], v[12:13]
	v_cvt_f32_f16_sdwa v13, v99 dst_sel:DWORD dst_unused:UNUSED_PAD src0_sel:WORD_1
	v_cvt_f32_f16_e32 v12, v99
	v_pk_add_f32 v[14:15], v[108:109], v[100:101]
	v_mov_b32_e32 v100, v9
	global_store_dwordx4 v[94:95], v[8:11], off offset:32
	v_pk_add_f32 v[12:13], v[106:107], v[12:13]
	global_store_dwordx4 v[94:95], v[12:15], off offset:48
	v_mov_b32_e32 v101, v13
	v_mov_b32_e32 v94, v8
	v_mov_b32_e32 v95, v12
	v_pk_mul_f32 v[100:101], v[100:101], v[100:101]
	v_add_f32_e32 v99, v102, v103
	v_pk_fma_f32 v[94:95], v[94:95], v[94:95], v[100:101]
	v_mov_b32_e32 v100, v10
	v_mov_b32_e32 v101, v14
	v_pk_fma_f32 v[94:95], v[100:101], v[100:101], v[94:95]
	v_mov_b32_e32 v100, v11
	v_mov_b32_e32 v101, v15
	v_pk_fma_f32 v[94:95], v[100:101], v[100:101], v[94:95]
	global_load_dwordx4 v[100:103], v[46:47], off offset:48
	global_load_dwordx4 v[104:107], v[46:47], off offset:32
	global_load_dwordx4 v[108:111], v[46:47], off offset:16
	global_load_dwordx4 v[112:115], v[46:47], off
	v_add_f32_e32 v94, v99, v94
	v_add_f32_e32 v94, v94, v95
	v_mov_b32_e32 v95, v94
	s_nop 1
	v_permlane32_swap_b32 v95, v94
	s_waitcnt lgkmcnt(0)
	v_add_f32_e32 v94, v94, v95
	v_mov_b32_e32 v95, v94
	s_nop 1
	v_permlane16_swap_b32 v95, v94
	s_waitcnt lgkmcnt(0)
	v_add_f32_e32 v94, v94, v95
	s_nop 1
	v_mov_b32_dpp v95, v94 row_ror:8 row_mask:0xf bank_mask:0xf
	s_waitcnt lgkmcnt(0)
	v_add_f32_e32 v94, v94, v95
	s_nop 1
	v_mov_b32_dpp v95, v94 row_half_mirror row_mask:0xf bank_mask:0xf
	s_nop 1
	v_mov_b32_dpp v95, v95 quad_perm:[3,2,1,0] row_mask:0xf bank_mask:0xf
	s_waitcnt lgkmcnt(0)
	v_add_f32_e32 v94, v94, v95
	s_nop 1
	v_mov_b32_dpp v95, v94 quad_perm:[2,3,0,1] row_mask:0xf bank_mask:0xf
	s_waitcnt lgkmcnt(0)
	v_add_f32_e32 v94, v94, v95
	s_nop 1
	v_mov_b32_dpp v95, v94 quad_perm:[1,0,3,2] row_mask:0xf bank_mask:0xf
	s_waitcnt lgkmcnt(0)
	v_add_f32_e32 v94, v94, v95
	v_fmamk_f32 v94, v94, 0x3a800000, v191
	v_cmp_gt_f32_e32 vcc, s12, v94
	v_mul_f32_e32 v95, 0x4b800000, v94
	s_nop 0
	v_cndmask_b32_e32 v94, v94, v95, vcc
	v_rsq_f32_e32 v94, v94
	s_nop 0
	v_mul_f32_e32 v95, 0x45800000, v94
	v_cndmask_b32_e32 v94, v94, v95, vcc
	v_pk_mul_f32 v[0:1], v[0:1], v[94:95] op_sel_hi:[1,0]
	v_pk_mul_f32 v[2:3], v[2:3], v[94:95] op_sel_hi:[1,0]
	s_waitcnt vmcnt(0)
	v_pk_mul_f32 v[0:1], v[112:113], v[0:1]
	v_pk_mul_f32 v[2:3], v[114:115], v[2:3]
	v_cvt_pk_bf16_f32 v0, v0, v1
	v_cvt_pk_bf16_f32 v1, v2, v3
	v_pk_mul_f32 v[2:3], v[4:5], v[94:95] op_sel_hi:[1,0]
	v_pk_mul_f32 v[4:5], v[6:7], v[94:95] op_sel_hi:[1,0]
	v_pk_mul_f32 v[2:3], v[108:109], v[2:3]
	v_pk_mul_f32 v[4:5], v[110:111], v[4:5]
	v_cvt_pk_bf16_f32 v2, v2, v3
	v_cvt_pk_bf16_f32 v3, v4, v5
	v_pk_mul_f32 v[4:5], v[8:9], v[94:95] op_sel_hi:[1,0]
	v_pk_mul_f32 v[6:7], v[10:11], v[94:95] op_sel_hi:[1,0]
	v_pk_mul_f32 v[4:5], v[104:105], v[4:5]
	v_pk_mul_f32 v[6:7], v[6:7], v[106:107]
	v_cvt_pk_bf16_f32 v4, v4, v5
	v_cvt_pk_bf16_f32 v5, v6, v7
	v_pk_mul_f32 v[6:7], v[12:13], v[94:95] op_sel_hi:[1,0]
	v_pk_mul_f32 v[8:9], v[14:15], v[94:95] op_sel_hi:[1,0]
	v_pk_mul_f32 v[6:7], v[6:7], v[100:101]
	v_pk_mul_f32 v[8:9], v[8:9], v[102:103]
	v_cvt_pk_bf16_f32 v6, v6, v7
	v_cvt_pk_bf16_f32 v7, v8, v9
	global_store_dwordx4 v[74:75], v[0:3], off
	global_store_dwordx4 v[74:75], v[4:7], off offset:16
	s_nop 0
	v_mov_b32_e32 v0, v98
	s_andn2_b64 exec, exec, s[8:9]
	s_cbranch_execnz .LBB0_769
